# adds 64-bit accumulator zeroing and moves the lagging half's re-offset barrier after its unit-top work (P8,P9) on top of the packed P8 epilogue, unit-top deferral and attention read pipelining
# baseline (speedup 1.0000x reference)
; template <class Epi, bool GATHER, int MODE, bool SPLIT = false>
; __device__ __forceinline__ void gemm_phase(PG8_LAS unsigned char* lds, const Gemm g, const Order& S, const Epi& E) {
;     ...
; #pragma unroll
;         for (int a = 0; a < 2; ++a)
; #pragma unroll
;             for (int b = 0; b < 2; ++b)
; #pragma unroll
;                 for (int m = 0; m < 4; ++m)
; #pragma unroll
;                     for (int n = 0; n < 2; ++n) acc[a][b][m][n] = (f32x4){0.f, 0.f, 0.f, 0.f};
;         cur = nxt; cB = nB; cAr = nAr; ++ui;
.LBB0_220:
	s_add_u32 s64, s19, s0
	s_addc_u32 s65, s21, s1
	s_add_u32 s7, s64, 0x40000
	s_addc_u32 s31, s65, 0
	s_add_u32 s66, s64, 0x60000
	s_addc_u32 s67, s65, 0
	s_add_u32 s68, s64, 0x20000
	s_addc_u32 s69, s65, 0
	s_mov_b32 s70, -2
	s_mov_b64 s[34:35], 0
	s_waitcnt vmcnt(18)
	s_waitcnt vmcnt(16)
	s_waitcnt vmcnt(14)
	s_waitcnt vmcnt(12)
	s_waitcnt vmcnt(10)
	s_waitcnt vmcnt(8)
	s_waitcnt vmcnt(7)
	s_waitcnt vmcnt(6)
	s_waitcnt vmcnt(4)
	s_waitcnt vmcnt(3)
	s_waitcnt vmcnt(2)
	v_mov_b64_e32 v[2:3], 0
	v_mov_b64_e32 v[4:5], 0
	v_mov_b64_e32 v[6:7], 0
	v_mov_b64_e32 v[8:9], 0
	v_mov_b64_e32 v[10:11], 0
	v_mov_b64_e32 v[12:13], 0
	v_mov_b64_e32 v[14:15], 0
	v_mov_b64_e32 v[16:17], 0
	v_mov_b64_e32 v[18:19], 0
	v_mov_b64_e32 v[20:21], 0
	v_mov_b64_e32 v[22:23], 0
	v_mov_b64_e32 v[24:25], 0
	v_mov_b64_e32 v[26:27], 0
	v_mov_b64_e32 v[28:29], 0
	v_mov_b64_e32 v[30:31], 0
	v_mov_b64_e32 v[32:33], 0
	v_mov_b64_e32 v[34:35], 0
	v_mov_b64_e32 v[36:37], 0
	v_mov_b64_e32 v[38:39], 0
	v_mov_b64_e32 v[40:41], 0
	v_mov_b64_e32 v[42:43], 0
	v_mov_b64_e32 v[44:45], 0
	v_mov_b64_e32 v[46:47], 0
	v_mov_b64_e32 v[48:49], 0
	v_mov_b64_e32 v[50:51], 0
	v_mov_b64_e32 v[52:53], 0
	v_mov_b64_e32 v[54:55], 0
	v_mov_b64_e32 v[56:57], 0
	v_mov_b64_e32 v[58:59], 0
	v_mov_b64_e32 v[60:61], 0
	v_mov_b64_e32 v[62:63], 0
	v_mov_b64_e32 v[64:65], 0
	v_mov_b64_e32 v[66:67], 0
	v_mov_b64_e32 v[68:69], 0
	v_mov_b64_e32 v[70:71], 0
	v_mov_b64_e32 v[72:73], 0
	v_mov_b64_e32 v[74:75], 0
	v_mov_b64_e32 v[76:77], 0
	v_mov_b64_e32 v[78:79], 0
	v_mov_b64_e32 v[80:81], 0
	v_mov_b64_e32 v[82:83], 0
	v_mov_b64_e32 v[84:85], 0
	v_mov_b64_e32 v[86:87], 0
	v_mov_b64_e32 v[88:89], 0
	v_mov_b64_e32 v[90:91], 0
	v_mov_b64_e32 v[92:93], 0
	v_mov_b64_e32 v[94:95], 0
	v_mov_b64_e32 v[96:97], 0
	v_mov_b64_e32 v[98:99], 0
	v_mov_b64_e32 v[100:101], 0
	v_mov_b64_e32 v[102:103], 0
	v_mov_b64_e32 v[104:105], 0
	v_mov_b64_e32 v[106:107], 0
	v_mov_b64_e32 v[108:109], 0
	v_mov_b64_e32 v[110:111], 0
	v_mov_b64_e32 v[112:113], 0
	v_mov_b64_e32 v[114:115], 0
	v_mov_b64_e32 v[116:117], 0
	v_mov_b64_e32 v[118:119], 0
	v_mov_b64_e32 v[120:121], 0
	v_mov_b64_e32 v[122:123], 0
	v_mov_b64_e32 v[124:125], 0
	v_mov_b64_e32 v[126:127], 0
	v_mov_b64_e32 v[128:129], 0

; #define PG8_STAGEA(bufoff, rowb, v, h, kb) do { if constexpr (GATHER) glds2((v)[h][0], Ab + (kb), (v)[h][1], Ab + (kb), ldsb + (bufoff)); \
;         else glds2(voffA, Ab + (rowb) + (h) * hstep + (kb), voffA, Ab + (rowb) + (h) * hstep + qstep + (kb), ldsb + (bufoff)); } while (0)
; #define PG8_LDA(dst, b, h) do { _Pragma("unroll") for (int m = 0; m < 4; ++m) _Pragma("unroll") for (int k = 0; k < 2; ++k) dst[m][k] = *(const PG8_LAS bf16x8*)(lds + PG8_SA(b, h) + aoff + m * 2048 + k * 1024); } while (0)
; #define PG8_LDB(dst, b, h) do { _Pragma("unroll") for (int n = 0; n < 2; ++n) _Pragma("unroll") for (int k = 0; k < 2; ++k) dst[n][k] = *(const PG8_LAS bf16x8*)(lds + PG8_SB(b, h) + boff + n * 2048 + k * 1024); } while (0)
; #define PG8_WAIT_V(n) asm volatile("s_waitcnt vmcnt(" #n ")" ::: "memory")
; #define PG8_WAIT_L(n) asm volatile("s_waitcnt lgkmcnt(" #n ")" ::: "memory")
; #define PG8_BAR __builtin_amdgcn_s_barrier()
; #define PG8_SCHED __builtin_amdgcn_sched_barrier(0)
; template <class Epi, bool GATHER, int MODE, bool SPLIT = false>
; __device__ __forceinline__ void gemm_phase(PG8_LAS unsigned char* lds, const Gemm g, const Order& S, const Epi& E) {
;     ...
;             const size_t k1 = (size_t)(t + 1) * kstep, k2 = k1 + kstep, k3 = k2 + kstep;
;             const char* b2 = cB + k2; const char* b3 = cB + k3;
;             PG8_LDB(B0, 0, 0); PG8_LDB(B1, 0, 1); PG8_SCHED; PG8_LDA(At, 0, 0); PG8_STAGEA(PG8_SA(1, 1), cAr, cv, 1, k1);
;             PG8_WAIT_V(8); PG8_WAIT_L(0); PG8_BAR; PG8_MMA(0, 0, At, B0); PG8_MMA(0, 1, At, B1); PG8_BAR; PG8_SCHED;
;     ...
; #pragma unroll
;         for (int a = 0; a < 2; ++a)
; #pragma unroll
;             for (int b = 0; b < 2; ++b)
; #pragma unroll
;                 for (int m = 0; m < 4; ++m)
; #pragma unroll
;                     for (int n = 0; n < 2; ++n) acc[a][b][m][n] = (f32x4){0.f, 0.f, 0.f, 0.f};
;         cur = nxt; cB = nB; cAr = nAr; ++ui;
; #pragma unroll
;         for (int h = 0; h < 2; ++h)
; #pragma unroll
;             for (int i = 0; i < 2; ++i) cv[h][i] = nv[h][i];
;         if (wr == 1) PG8_BAR;
.LBB0_801:
	s_mov_b32 s11, -2
	s_mov_b64 s[30:31], 0
	v_mov_b64_e32 v[2:3], 0
	v_mov_b64_e32 v[4:5], 0
	v_mov_b64_e32 v[6:7], 0
	v_mov_b64_e32 v[8:9], 0
	v_mov_b64_e32 v[10:11], 0
	v_mov_b64_e32 v[12:13], 0
	v_mov_b64_e32 v[14:15], 0
	v_mov_b64_e32 v[16:17], 0
	v_mov_b64_e32 v[18:19], 0
	v_mov_b64_e32 v[20:21], 0
	v_mov_b64_e32 v[22:23], 0
	v_mov_b64_e32 v[24:25], 0
	v_mov_b64_e32 v[26:27], 0
	v_mov_b64_e32 v[28:29], 0
	v_mov_b64_e32 v[30:31], 0
	v_mov_b64_e32 v[32:33], 0
	v_mov_b64_e32 v[34:35], 0
	v_mov_b64_e32 v[36:37], 0
	v_mov_b64_e32 v[38:39], 0
	v_mov_b64_e32 v[40:41], 0
	v_mov_b64_e32 v[42:43], 0
	v_mov_b64_e32 v[44:45], 0
	v_mov_b64_e32 v[46:47], 0
	v_mov_b64_e32 v[48:49], 0
	v_mov_b64_e32 v[50:51], 0
	v_mov_b64_e32 v[52:53], 0
	v_mov_b64_e32 v[54:55], 0
	v_mov_b64_e32 v[56:57], 0
	v_mov_b64_e32 v[58:59], 0
	v_mov_b64_e32 v[60:61], 0
	v_mov_b64_e32 v[62:63], 0
	v_mov_b64_e32 v[64:65], 0
	v_mov_b64_e32 v[66:67], 0
	v_mov_b64_e32 v[68:69], 0
	v_mov_b64_e32 v[70:71], 0
	v_mov_b64_e32 v[72:73], 0
	v_mov_b64_e32 v[74:75], 0
	v_mov_b64_e32 v[76:77], 0
	v_mov_b64_e32 v[78:79], 0
	v_mov_b64_e32 v[80:81], 0
	v_mov_b64_e32 v[82:83], 0
	v_mov_b64_e32 v[84:85], 0
	v_mov_b64_e32 v[86:87], 0
	v_mov_b64_e32 v[88:89], 0
	v_mov_b64_e32 v[90:91], 0
	v_mov_b64_e32 v[92:93], 0
	v_mov_b64_e32 v[94:95], 0
	v_mov_b64_e32 v[96:97], 0
	v_mov_b64_e32 v[98:99], 0
	v_mov_b64_e32 v[100:101], 0
	v_mov_b64_e32 v[102:103], 0
	v_mov_b64_e32 v[104:105], 0
	v_mov_b64_e32 v[106:107], 0
	v_mov_b64_e32 v[108:109], 0
	v_mov_b64_e32 v[110:111], 0
	v_mov_b64_e32 v[112:113], 0
	v_mov_b64_e32 v[114:115], 0
	v_mov_b64_e32 v[116:117], 0
	v_mov_b64_e32 v[118:119], 0
	v_mov_b64_e32 v[120:121], 0
	v_mov_b64_e32 v[122:123], 0
	v_mov_b64_e32 v[124:125], 0
	v_mov_b64_e32 v[126:127], 0
	v_mov_b64_e32 v[128:129], 0
	s_cmp_lt_u32 s47, 2
	s_cbranch_scc1 .Lp8_nobar
	s_andn2_b64 vcc, exec, s[12:13]
	s_cbranch_vccnz .Lp8_nobar
	s_barrier
.Lp8_nobar:
.LBB0_802:
	ds_read_b128 v[158:161], v179
	ds_read_b128 v[150:153], v179 offset:1024
	ds_read_b128 v[154:157], v179 offset:2048
	ds_read_b128 v[146:149], v179 offset:3072
	ds_read_b128 v[142:145], v180
	ds_read_b128 v[130:133], v180 offset:1024
	ds_read_b128 v[138:141], v180 offset:2048
	ds_read_b128 v[134:137], v180 offset:3072
	s_add_u32 s66, s34, s30
	s_addc_u32 s67, s35, s31
	s_add_u32 s36, s66, 0x100
	s_addc_u32 s37, s67, 0
	ds_read_b128 v[194:197], v181
	ds_read_b128 v[198:201], v181 offset:1024
	ds_read_b128 v[202:205], v181 offset:2048
	ds_read_b128 v[206:209], v181 offset:3072
	ds_read_b128 v[210:213], v181 offset:4096
	ds_read_b128 v[214:217], v181 offset:5120
	ds_read_b128 v[218:221], v181 offset:6144
	ds_read_b128 v[222:225], v181 offset:7168
	s_add_u32 s27, s6, s30
	s_addc_u32 s29, s7, s31
	s_add_u32 s68, s27, 0x80
	s_addc_u32 s69, s29, 0
	s_mov_b32 s70, m0
	s_mov_b32 m0, s62
	s_nop 0
	global_load_lds_dwordx4 v189, s[68:69]
	s_mov_b32 m0, s63
	s_nop 0
	global_load_lds_dwordx4 v190, s[68:69]
	s_mov_b32 m0, s70
	s_waitcnt vmcnt(8)
	s_waitcnt lgkmcnt(0)
	s_barrier
	s_setprio 1
	s_waitcnt lgkmcnt(7)
	v_mfma_i32_16x16x64_i8 v[126:129], v[158:161], v[194:197], v[126:129]
	v_mfma_i32_16x16x64_i8 v[122:125], v[154:157], v[194:197], v[122:125]
	s_waitcnt lgkmcnt(5)
	v_mfma_i32_16x16x64_i8 v[118:121], v[158:161], v[202:205], v[118:121]
	v_mfma_i32_16x16x64_i8 v[106:109], v[154:157], v[202:205], v[106:109]
	s_waitcnt lgkmcnt(3)
	v_mfma_i32_16x16x64_i8 v[102:105], v[158:161], v[210:213], v[102:105]
	v_mfma_i32_16x16x64_i8 v[90:93], v[154:157], v[210:213], v[90:93]
	s_waitcnt lgkmcnt(1)
	v_mfma_i32_16x16x64_i8 v[86:89], v[158:161], v[218:221], v[86:89]
	v_mfma_i32_16x16x64_i8 v[74:77], v[154:157], v[218:221], v[74:77]
	v_mfma_i32_16x16x64_i8 v[126:129], v[150:153], v[198:201], v[126:129]
	v_mfma_i32_16x16x64_i8 v[122:125], v[146:149], v[198:201], v[122:125]
	v_mfma_i32_16x16x64_i8 v[118:121], v[150:153], v[206:209], v[118:121]
	v_mfma_i32_16x16x64_i8 v[106:109], v[146:149], v[206:209], v[106:109]
	v_mfma_i32_16x16x64_i8 v[102:105], v[150:153], v[214:217], v[102:105]
	v_mfma_i32_16x16x64_i8 v[90:93], v[146:149], v[214:217], v[90:93]
	s_waitcnt lgkmcnt(0)
	v_mfma_i32_16x16x64_i8 v[86:89], v[150:153], v[222:225], v[86:89]
	v_mfma_i32_16x16x64_i8 v[74:77], v[146:149], v[222:225], v[74:77]
	s_setprio 0
	s_setprio 1
	v_mfma_i32_16x16x64_i8 v[114:117], v[142:145], v[194:197], v[114:117]
	v_mfma_i32_16x16x64_i8 v[110:113], v[138:141], v[194:197], v[110:113]
	v_mfma_i32_16x16x64_i8 v[98:101], v[142:145], v[202:205], v[98:101]
	v_mfma_i32_16x16x64_i8 v[94:97], v[138:141], v[202:205], v[94:97]
	v_mfma_i32_16x16x64_i8 v[82:85], v[142:145], v[210:213], v[82:85]
	v_mfma_i32_16x16x64_i8 v[78:81], v[138:141], v[210:213], v[78:81]
	v_mfma_i32_16x16x64_i8 v[70:73], v[142:145], v[218:221], v[70:73]
	v_mfma_i32_16x16x64_i8 v[66:69], v[138:141], v[218:221], v[66:69]
	s_nop 0
	v_mfma_i32_16x16x64_i8 v[114:117], v[130:133], v[198:201], v[114:117]
	v_mfma_i32_16x16x64_i8 v[110:113], v[134:137], v[198:201], v[110:113]
	v_mfma_i32_16x16x64_i8 v[98:101], v[130:133], v[206:209], v[98:101]
	v_mfma_i32_16x16x64_i8 v[94:97], v[134:137], v[206:209], v[94:97]
	v_mfma_i32_16x16x64_i8 v[82:85], v[130:133], v[214:217], v[82:85]
	v_mfma_i32_16x16x64_i8 v[78:81], v[134:137], v[214:217], v[78:81]
	v_mfma_i32_16x16x64_i8 v[70:73], v[130:133], v[222:225], v[70:73]
	v_mfma_i32_16x16x64_i8 v[66:69], v[134:137], v[222:225], v[66:69]
	s_setprio 0
	s_barrier
; #define PG8_STAGEB(bufoff, gbase) glds2(voffB, (gbase), voffB, (gbase) + qstep, ldsb + (bufoff))
; #define PG8_STAGEA(bufoff, rowb, v, h, kb) do { if constexpr (GATHER) glds2((v)[h][0], Ab + (kb), (v)[h][1], Ab + (kb), ldsb + (bufoff)); \
;         else glds2(voffA, Ab + (rowb) + (h) * hstep + (kb), voffA, Ab + (rowb) + (h) * hstep + qstep + (kb), ldsb + (bufoff)); } while (0)
; #define PG8_LDA(dst, b, h) do { _Pragma("unroll") for (int m = 0; m < 4; ++m) _Pragma("unroll") for (int k = 0; k < 2; ++k) dst[m][k] = *(const PG8_LAS bf16x8*)(lds + PG8_SA(b, h) + aoff + m * 2048 + k * 1024); } while (0)
; #define PG8_LDB(dst, b, h) do { _Pragma("unroll") for (int n = 0; n < 2; ++n) _Pragma("unroll") for (int k = 0; k < 2; ++k) dst[n][k] = *(const PG8_LAS bf16x8*)(lds + PG8_SB(b, h) + boff + n * 2048 + k * 1024); } while (0)
; #define PG8_WAIT_V(n) asm volatile("s_waitcnt vmcnt(" #n ")" ::: "memory")
; #define PG8_WAIT_L(n) asm volatile("s_waitcnt lgkmcnt(" #n ")" ::: "memory")
; #define PG8_BAR __builtin_amdgcn_s_barrier()
; #define PG8_SCHED __builtin_amdgcn_sched_barrier(0)
; template <class Epi, bool GATHER, int MODE, bool SPLIT = false>
; __device__ __forceinline__ void gemm_phase(PG8_LAS unsigned char* lds, const Gemm g, const Order& S, const Epi& E) {
;     ...
;             PG8_LDA(At, 0, 1); PG8_STAGEB(PG8_SB(0, 0), b2); PG8_STAGEB(PG8_SB(0, 1), b2 + hstep); PG8_STAGEA(PG8_SA(0, 0), cAr, cv, 0, k2);
;             PG8_WAIT_V(8); PG8_WAIT_L(0); PG8_BAR; PG8_MMA(1, 0, At, B0); PG8_MMA(1, 1, At, B1); PG8_BAR; PG8_SCHED;
;             PG8_LDB(B0, 1, 0); PG8_LDB(B1, 1, 1); PG8_SCHED; PG8_LDA(At, 1, 0); PG8_STAGEA(PG8_SA(0, 1), cAr, cv, 1, k2);
;             PG8_WAIT_V(8); PG8_WAIT_L(0); PG8_BAR; PG8_MMA(0, 0, At, B0); PG8_MMA(0, 1, At, B1); PG8_BAR; PG8_SCHED;
	s_add_u32 s68, s66, 0x20100
	s_addc_u32 s69, s67, 0
	ds_read_b128 v[194:197], v181 offset:16384
	ds_read_b128 v[198:201], v181 offset:17408
	ds_read_b128 v[202:205], v181 offset:18432
	ds_read_b128 v[206:209], v181 offset:19456
	ds_read_b128 v[210:213], v181 offset:20480
	ds_read_b128 v[214:217], v181 offset:21504
	ds_read_b128 v[218:221], v181 offset:22528
	ds_read_b128 v[222:225], v181 offset:23552
	s_mov_b32 s70, m0
	s_mov_b32 m0, s49
	s_nop 0
	global_load_lds_dwordx4 v168, s[36:37]
	s_mov_b32 m0, s50
	s_nop 0
	global_load_lds_dwordx4 v168, s[68:69]
	s_mov_b32 m0, s70
	s_add_u32 s36, s66, 0x40100
	s_addc_u32 s37, s67, 0
	s_add_u32 s68, s66, 0x60100
	s_addc_u32 s69, s67, 0
	s_mov_b32 s70, m0
	s_mov_b32 m0, s51
	s_nop 0
	global_load_lds_dwordx4 v168, s[36:37]
	s_mov_b32 m0, s52
	s_nop 0
	global_load_lds_dwordx4 v168, s[68:69]
	s_mov_b32 m0, s70
	s_add_u32 s36, s27, 0x100
	s_addc_u32 s37, s29, 0
	s_mov_b32 s68, m0
	s_mov_b32 m0, s43
	s_nop 0
	global_load_lds_dwordx4 v191, s[36:37]
	s_mov_b32 m0, s53
	s_nop 0
	global_load_lds_dwordx4 v192, s[36:37]
	s_mov_b32 m0, s68
	s_waitcnt vmcnt(8)
	s_waitcnt lgkmcnt(0)
	s_barrier
	s_setprio 1
	s_waitcnt lgkmcnt(7)
	v_mfma_i32_16x16x64_i8 v[62:65], v[158:161], v[194:197], v[62:65]
	v_mfma_i32_16x16x64_i8 v[58:61], v[154:157], v[194:197], v[58:61]
	s_waitcnt lgkmcnt(5)
	v_mfma_i32_16x16x64_i8 v[46:49], v[158:161], v[202:205], v[46:49]
	v_mfma_i32_16x16x64_i8 v[42:45], v[154:157], v[202:205], v[42:45]
	s_waitcnt lgkmcnt(3)
	v_mfma_i32_16x16x64_i8 v[38:41], v[158:161], v[210:213], v[38:41]
	v_mfma_i32_16x16x64_i8 v[34:37], v[154:157], v[210:213], v[34:37]
	s_waitcnt lgkmcnt(1)
	v_mfma_i32_16x16x64_i8 v[22:25], v[158:161], v[218:221], v[22:25]
	v_mfma_i32_16x16x64_i8 v[18:21], v[154:157], v[218:221], v[18:21]
	v_mfma_i32_16x16x64_i8 v[62:65], v[150:153], v[198:201], v[62:65]
	v_mfma_i32_16x16x64_i8 v[58:61], v[146:149], v[198:201], v[58:61]
	v_mfma_i32_16x16x64_i8 v[46:49], v[150:153], v[206:209], v[46:49]
	v_mfma_i32_16x16x64_i8 v[42:45], v[146:149], v[206:209], v[42:45]
	v_mfma_i32_16x16x64_i8 v[38:41], v[150:153], v[214:217], v[38:41]
	v_mfma_i32_16x16x64_i8 v[34:37], v[146:149], v[214:217], v[34:37]
	s_waitcnt lgkmcnt(0)
	v_mfma_i32_16x16x64_i8 v[22:25], v[150:153], v[222:225], v[22:25]
	v_mfma_i32_16x16x64_i8 v[18:21], v[146:149], v[222:225], v[18:21]
	s_setprio 0
	s_setprio 1
	v_mfma_i32_16x16x64_i8 v[54:57], v[142:145], v[194:197], v[54:57]
	v_mfma_i32_16x16x64_i8 v[50:53], v[138:141], v[194:197], v[50:53]
	v_mfma_i32_16x16x64_i8 v[30:33], v[142:145], v[202:205], v[30:33]
	v_mfma_i32_16x16x64_i8 v[26:29], v[138:141], v[202:205], v[26:29]
	v_mfma_i32_16x16x64_i8 v[14:17], v[142:145], v[210:213], v[14:17]
	v_mfma_i32_16x16x64_i8 v[10:13], v[138:141], v[210:213], v[10:13]
	v_mfma_i32_16x16x64_i8 v[6:9], v[142:145], v[218:221], v[6:9]
	v_mfma_i32_16x16x64_i8 v[2:5], v[138:141], v[218:221], v[2:5]
	s_nop 0
	v_mfma_i32_16x16x64_i8 v[54:57], v[130:133], v[198:201], v[54:57]
	v_mfma_i32_16x16x64_i8 v[50:53], v[134:137], v[198:201], v[50:53]
	v_mfma_i32_16x16x64_i8 v[30:33], v[130:133], v[206:209], v[30:33]
	v_mfma_i32_16x16x64_i8 v[26:29], v[134:137], v[206:209], v[26:29]
	v_mfma_i32_16x16x64_i8 v[14:17], v[130:133], v[214:217], v[14:17]
	v_mfma_i32_16x16x64_i8 v[10:13], v[134:137], v[214:217], v[10:13]
	v_mfma_i32_16x16x64_i8 v[6:9], v[130:133], v[222:225], v[6:9]
	v_mfma_i32_16x16x64_i8 v[2:5], v[134:137], v[222:225], v[2:5]
	s_setprio 0
	s_barrier
	v_add_u32_e32 v138, 0x1c000, v178
	ds_read_b128 v[130:133], v182
	ds_read_b128 v[134:137], v182 offset:1024
	ds_read_b128 v[140:143], v182 offset:2048
	ds_read_b128 v[144:147], v182 offset:3072
	ds_read_b128 v[148:151], v138
	ds_read_b128 v[152:155], v138 offset:1024
	ds_read_b128 v[156:159], v138 offset:2048
	ds_read_b128 v[194:197], v138 offset:3072
	ds_read_b128 v[198:201], v181 offset:32768
	ds_read_b128 v[202:205], v181 offset:33792
	ds_read_b128 v[206:209], v181 offset:34816
	ds_read_b128 v[210:213], v181 offset:35840
	ds_read_b128 v[214:217], v181 offset:36864
	ds_read_b128 v[218:221], v181 offset:37888
	ds_read_b128 v[222:225], v181 offset:38912
	ds_read_b128 v[226:229], v181 offset:39936
	s_mov_b32 s68, m0
	s_mov_b32 m0, s54
	s_nop 0
	global_load_lds_dwordx4 v189, s[36:37]
	s_mov_b32 m0, s55
	s_nop 0
	global_load_lds_dwordx4 v190, s[36:37]
	s_mov_b32 m0, s68
	s_waitcnt vmcnt(8)
	s_waitcnt lgkmcnt(0)
	s_barrier
; #define PG8_STAGEB(bufoff, gbase) glds2(voffB, (gbase), voffB, (gbase) + qstep, ldsb + (bufoff))
; #define PG8_STAGEA(bufoff, rowb, v, h, kb) do { if constexpr (GATHER) glds2((v)[h][0], Ab + (kb), (v)[h][1], Ab + (kb), ldsb + (bufoff)); \
;         else glds2(voffA, Ab + (rowb) + (h) * hstep + (kb), voffA, Ab + (rowb) + (h) * hstep + qstep + (kb), ldsb + (bufoff)); } while (0)
; #define PG8_LDA(dst, b, h) do { _Pragma("unroll") for (int m = 0; m < 4; ++m) _Pragma("unroll") for (int k = 0; k < 2; ++k) dst[m][k] = *(const PG8_LAS bf16x8*)(lds + PG8_SA(b, h) + aoff + m * 2048 + k * 1024); } while (0)
; #define PG8_WAIT_V(n) asm volatile("s_waitcnt vmcnt(" #n ")" ::: "memory")
; #define PG8_WAIT_L(n) asm volatile("s_waitcnt lgkmcnt(" #n ")" ::: "memory")
; #define PG8_BAR __builtin_amdgcn_s_barrier()
; #define PG8_SCHED __builtin_amdgcn_sched_barrier(0)
; #define PG8_VOFF(dst, U) do { if constexpr (GATHER) { _Pragma("unroll") for (int h = 0; h < 2; ++h) _Pragma("unroll") for (int i = 0; i < 2; ++i) { \
;         const int row = g.rowidx[(U).pm * BM + h * HALF + i * 64 + R0]; dst[h][i] = (unsigned)row * (unsigned)RB + (unsigned)C0 * 2u; } } } while (0)
; template <class Epi, bool GATHER, int MODE, bool SPLIT = false>
; __device__ __forceinline__ void gemm_phase(PG8_LAS unsigned char* lds, const Gemm g, const Order& S, const Epi& E) {
;     ...
;         const bool has_next = S.next(ui + 1, nxt);
;         const char* nB = has_next ? (const char*)g.Bt + (size_t)nxt.e * g.bstride + (size_t)nxt.pn * tstep : cB;
;         const size_t nAr = has_next ? (size_t)nxt.pm * tstep : cAr;
;         if (has_next) { PG8_VOFF(nv, nxt); }
;     ...
;             PG8_WAIT_V(8); PG8_WAIT_L(0); PG8_BAR; PG8_MMA(0, 0, At, B0); PG8_MMA(0, 1, At, B1); PG8_BAR; PG8_SCHED;
;             PG8_LDA(At, 1, 1); PG8_STAGEB(PG8_SB(1, 0), b3); PG8_STAGEB(PG8_SB(1, 1), b3 + hstep); PG8_STAGEA(PG8_SA(1, 0), cAr, cv, 0, k3);
;             PG8_WAIT_V(8); PG8_WAIT_L(0); PG8_BAR; PG8_MMA(1, 0, At, B0); PG8_MMA(1, 1, At, B1); PG8_BAR; PG8_SCHED;
;         }
	s_setprio 1
	s_waitcnt lgkmcnt(7)
	v_mfma_i32_16x16x64_i8 v[126:129], v[130:133], v[198:201], v[126:129]
	v_mfma_i32_16x16x64_i8 v[122:125], v[140:143], v[198:201], v[122:125]
	s_waitcnt lgkmcnt(5)
	v_mfma_i32_16x16x64_i8 v[118:121], v[130:133], v[206:209], v[118:121]
	v_mfma_i32_16x16x64_i8 v[106:109], v[140:143], v[206:209], v[106:109]
	s_waitcnt lgkmcnt(3)
	v_mfma_i32_16x16x64_i8 v[102:105], v[130:133], v[214:217], v[102:105]
	v_mfma_i32_16x16x64_i8 v[90:93], v[140:143], v[214:217], v[90:93]
	s_waitcnt lgkmcnt(1)
	v_mfma_i32_16x16x64_i8 v[86:89], v[130:133], v[222:225], v[86:89]
	v_mfma_i32_16x16x64_i8 v[74:77], v[140:143], v[222:225], v[74:77]
	v_mfma_i32_16x16x64_i8 v[126:129], v[134:137], v[202:205], v[126:129]
	v_mfma_i32_16x16x64_i8 v[122:125], v[144:147], v[202:205], v[122:125]
	v_mfma_i32_16x16x64_i8 v[118:121], v[134:137], v[210:213], v[118:121]
	v_mfma_i32_16x16x64_i8 v[106:109], v[144:147], v[210:213], v[106:109]
	v_mfma_i32_16x16x64_i8 v[102:105], v[134:137], v[218:221], v[102:105]
	v_mfma_i32_16x16x64_i8 v[90:93], v[144:147], v[218:221], v[90:93]
	s_waitcnt lgkmcnt(0)
	v_mfma_i32_16x16x64_i8 v[86:89], v[134:137], v[226:229], v[86:89]
	v_mfma_i32_16x16x64_i8 v[74:77], v[144:147], v[226:229], v[74:77]
	s_setprio 0
	s_setprio 1
	v_mfma_i32_16x16x64_i8 v[114:117], v[148:151], v[198:201], v[114:117]
	v_mfma_i32_16x16x64_i8 v[110:113], v[156:159], v[198:201], v[110:113]
	v_mfma_i32_16x16x64_i8 v[98:101], v[148:151], v[206:209], v[98:101]
	v_mfma_i32_16x16x64_i8 v[94:97], v[156:159], v[206:209], v[94:97]
	v_mfma_i32_16x16x64_i8 v[82:85], v[148:151], v[214:217], v[82:85]
	v_mfma_i32_16x16x64_i8 v[78:81], v[156:159], v[214:217], v[78:81]
	v_mfma_i32_16x16x64_i8 v[70:73], v[148:151], v[222:225], v[70:73]
	v_mfma_i32_16x16x64_i8 v[66:69], v[156:159], v[222:225], v[66:69]
	s_nop 0
	v_mfma_i32_16x16x64_i8 v[114:117], v[152:155], v[202:205], v[114:117]
	v_mfma_i32_16x16x64_i8 v[110:113], v[194:197], v[202:205], v[110:113]
	v_mfma_i32_16x16x64_i8 v[98:101], v[152:155], v[210:213], v[98:101]
	v_mfma_i32_16x16x64_i8 v[94:97], v[194:197], v[210:213], v[94:97]
	v_mfma_i32_16x16x64_i8 v[82:85], v[152:155], v[218:221], v[82:85]
	v_mfma_i32_16x16x64_i8 v[78:81], v[194:197], v[218:221], v[78:81]
	v_mfma_i32_16x16x64_i8 v[70:73], v[152:155], v[226:229], v[70:73]
	v_mfma_i32_16x16x64_i8 v[66:69], v[194:197], v[226:229], v[66:69]
	s_setprio 0
	s_barrier
	s_add_u32 s36, s66, 0x180
	s_addc_u32 s37, s67, 0
	s_add_u32 s68, s66, 0x20180
	s_addc_u32 s69, s67, 0
	ds_read_b128 v[198:201], v181 offset:49152
	ds_read_b128 v[202:205], v181 offset:50176
	ds_read_b128 v[206:209], v181 offset:51200
	ds_read_b128 v[210:213], v181 offset:52224
	ds_read_b128 v[214:217], v181 offset:53248
	ds_read_b128 v[218:221], v181 offset:54272
	ds_read_b128 v[222:225], v181 offset:55296
	ds_read_b128 v[226:229], v181 offset:56320
	s_mov_b32 s70, m0
	s_mov_b32 m0, s56
	s_nop 0
	global_load_lds_dwordx4 v168, s[36:37]
	s_mov_b32 m0, s57
	s_nop 0
	global_load_lds_dwordx4 v168, s[68:69]
	s_mov_b32 m0, s70
	s_add_u32 s36, s66, 0x40180
	s_addc_u32 s37, s67, 0
	s_add_u32 s66, s66, 0x60180
	s_addc_u32 s67, s67, 0
	s_mov_b32 s68, m0
	s_mov_b32 m0, s60
	s_nop 0
	global_load_lds_dwordx4 v168, s[36:37]
	s_mov_b32 m0, s61
	s_nop 0
	global_load_lds_dwordx4 v168, s[66:67]
	s_mov_b32 m0, s68
	s_add_u32 s36, s27, 0x180
	s_addc_u32 s37, s29, 0
	s_mov_b32 s27, m0
	s_mov_b32 m0, s58
	s_nop 0
	global_load_lds_dwordx4 v191, s[36:37]
	s_mov_b32 m0, s59
	s_nop 0
	global_load_lds_dwordx4 v192, s[36:37]
	s_mov_b32 m0, s27
	s_waitcnt vmcnt(8)
	s_waitcnt lgkmcnt(0)
	s_barrier
	s_setprio 1
	s_waitcnt lgkmcnt(7)
	v_mfma_i32_16x16x64_i8 v[62:65], v[130:133], v[198:201], v[62:65]
	v_mfma_i32_16x16x64_i8 v[58:61], v[140:143], v[198:201], v[58:61]
	s_waitcnt lgkmcnt(5)
	v_mfma_i32_16x16x64_i8 v[46:49], v[130:133], v[206:209], v[46:49]
	v_mfma_i32_16x16x64_i8 v[42:45], v[140:143], v[206:209], v[42:45]
	s_waitcnt lgkmcnt(3)
	v_mfma_i32_16x16x64_i8 v[38:41], v[130:133], v[214:217], v[38:41]
	v_mfma_i32_16x16x64_i8 v[34:37], v[140:143], v[214:217], v[34:37]
	s_waitcnt lgkmcnt(1)
	v_mfma_i32_16x16x64_i8 v[22:25], v[130:133], v[222:225], v[22:25]
	v_mfma_i32_16x16x64_i8 v[18:21], v[140:143], v[222:225], v[18:21]
	v_mfma_i32_16x16x64_i8 v[62:65], v[134:137], v[202:205], v[62:65]
	v_mfma_i32_16x16x64_i8 v[58:61], v[144:147], v[202:205], v[58:61]
	v_mfma_i32_16x16x64_i8 v[46:49], v[134:137], v[210:213], v[46:49]
	v_mfma_i32_16x16x64_i8 v[42:45], v[144:147], v[210:213], v[42:45]
	v_mfma_i32_16x16x64_i8 v[38:41], v[134:137], v[218:221], v[38:41]
	v_mfma_i32_16x16x64_i8 v[34:37], v[144:147], v[218:221], v[34:37]
	s_waitcnt lgkmcnt(0)
	v_mfma_i32_16x16x64_i8 v[22:25], v[134:137], v[226:229], v[22:25]
	v_mfma_i32_16x16x64_i8 v[18:21], v[144:147], v[226:229], v[18:21]
	s_setprio 0
	s_setprio 1
	v_mfma_i32_16x16x64_i8 v[54:57], v[148:151], v[198:201], v[54:57]
	v_mfma_i32_16x16x64_i8 v[50:53], v[156:159], v[198:201], v[50:53]
	v_mfma_i32_16x16x64_i8 v[30:33], v[148:151], v[206:209], v[30:33]
	v_mfma_i32_16x16x64_i8 v[26:29], v[156:159], v[206:209], v[26:29]
	v_mfma_i32_16x16x64_i8 v[14:17], v[148:151], v[214:217], v[14:17]
	v_mfma_i32_16x16x64_i8 v[10:13], v[156:159], v[214:217], v[10:13]
	v_mfma_i32_16x16x64_i8 v[6:9], v[148:151], v[222:225], v[6:9]
	v_mfma_i32_16x16x64_i8 v[2:5], v[156:159], v[222:225], v[2:5]
	s_nop 0
	v_mfma_i32_16x16x64_i8 v[54:57], v[152:155], v[202:205], v[54:57]
	v_mfma_i32_16x16x64_i8 v[50:53], v[194:197], v[202:205], v[50:53]
	v_mfma_i32_16x16x64_i8 v[30:33], v[152:155], v[210:213], v[30:33]
	v_mfma_i32_16x16x64_i8 v[26:29], v[194:197], v[210:213], v[26:29]
	v_mfma_i32_16x16x64_i8 v[14:17], v[152:155], v[218:221], v[14:17]
	v_mfma_i32_16x16x64_i8 v[10:13], v[194:197], v[218:221], v[10:13]
	v_mfma_i32_16x16x64_i8 v[6:9], v[152:155], v[226:229], v[6:9]
	v_mfma_i32_16x16x64_i8 v[2:5], v[194:197], v[226:229], v[2:5]
	s_setprio 0
	s_barrier
	s_add_i32 s11, s11, 2
	s_add_u32 s30, s30, 0x100
	s_addc_u32 s31, s31, 0
	s_cmp_lt_u32 s11, 12
	s_cbranch_scc1 .LBB0_802
	v_readfirstlane_b32 s28, v230
	s_and_b64 s[98:99], s[4:5], exec
	s_cbranch_scc0 .Lp8_nonext
	v_lshl_add_u32 v184, v231, 11, v167
	v_lshl_add_u32 v185, v232, 11, v167
	v_lshl_add_u32 v186, v233, 11, v167
	v_lshl_add_u32 v187, v234, 11, v167

;     __device__ __forceinline__ void operator()(const f32x4 (&acc)[2][2][4][2], const Unit& u, int wr, int wc, int fr, int fq) const {
;         const int row0 = u.pm * BM + wr * 64 + fr, col = u.pn * 128 + wc * 32 + 8 * fq;
;         const float* bg = bgu + (size_t)u.e * (2 * DFF) + col;
;         const f32x4 g0 = *(const f32x4*)bg, g1 = *(const f32x4*)(bg + 4), u0 = *(const f32x4*)(bg + DFF), u1 = *(const f32x4*)(bg + DFF + 4);
;         const int colw = col & ~8, odd = fq & 1;
; template <class Epi, bool GATHER, int MODE, bool SPLIT = false>
; __device__ __forceinline__ void gemm_phase(PG8_LAS unsigned char* lds, const Gemm g, const Order& S, const Epi& E) {
;     ...
;         if constexpr (MODE == 2) {
; #pragma unroll
;             for (int a = 0; a < 2; ++a)
; #pragma unroll
;                 for (int m = 0; m < 4; ++m) { const float rs = __builtin_bit_cast(float, __builtin_amdgcn_ds_bpermute((m * 16 + fr) * 4, __builtin_bit_cast(int, rs2[a])));
; #pragma unroll
;                     for (int b = 0; b < 2; ++b)
; #pragma unroll
;                         for (int n = 0; n < 2; ++n) { const v4i_t iv = __builtin_bit_cast(v4i_t, acc[a][b][m][n]); acc[a][b][m][n] = (f32x4){(float)iv[0], (float)iv[1], (float)iv[2], (float)iv[3]} * rs; } }
;         }
.LBB0_805:
	s_waitcnt vmcnt(0)
	s_nop 7
	ds_bpermute_b32 v194, v170, v165
	ds_bpermute_b32 v196, v174, v165
	ds_bpermute_b32 v198, v175, v165
	ds_bpermute_b32 v200, v176, v165
	ds_bpermute_b32 v202, v170, v188
	ds_bpermute_b32 v204, v174, v188
	ds_bpermute_b32 v206, v175, v188
	ds_bpermute_b32 v208, v176, v188
	s_lshl_b32 s0, s0, 7
	s_mov_b32 s98, 0xc01d265f
	v_ashrrev_i32_e32 v149, 31, v164
	v_mov_b32_e32 v148, v164
	v_or_b32_e32 v150, s0, v177
	v_lshlrev_b64 v[148:149], 14, v[148:149]
	v_ashrrev_i32_e32 v151, 31, v150
	v_lshl_add_u64 v[148:149], s[84:85], 0, v[148:149]
	v_lshl_add_u64 v[148:149], v[150:151], 2, v[148:149]
	v_lshl_add_u64 v[150:151], v[148:149], 0, s[24:25]
	global_load_dwordx4 v[132:135], v[148:149], off
	global_load_dwordx4 v[136:139], v[148:149], off offset:16
	global_load_dwordx4 v[140:143], v[150:151], off
	global_load_dwordx4 v[144:147], v[150:151], off offset:16
	v_bitop3_b32 v234, s0, -16, v177 bitop3:0xc8
	v_add_u32_e32 v232, s1, v169
	v_ashrrev_i32_e32 v235, 31, v234
	v_add_u32_e32 v233, 0x80, v232
	v_cvt_f32_i32_e32 v126, v126
	v_cvt_f32_i32_e32 v127, v127
	v_cvt_f32_i32_e32 v128, v128
	v_cvt_f32_i32_e32 v129, v129
	v_cvt_f32_i32_e32 v122, v122
	v_cvt_f32_i32_e32 v123, v123
	v_cvt_f32_i32_e32 v124, v124
	v_cvt_f32_i32_e32 v125, v125
	v_cvt_f32_i32_e32 v118, v118
	v_cvt_f32_i32_e32 v119, v119
	v_cvt_f32_i32_e32 v120, v120
	v_cvt_f32_i32_e32 v121, v121
	v_cvt_f32_i32_e32 v106, v106
	v_cvt_f32_i32_e32 v107, v107
	v_cvt_f32_i32_e32 v108, v108
	v_cvt_f32_i32_e32 v109, v109
	v_cvt_f32_i32_e32 v102, v102
	v_cvt_f32_i32_e32 v103, v103
	v_cvt_f32_i32_e32 v104, v104
	v_cvt_f32_i32_e32 v105, v105
	v_cvt_f32_i32_e32 v90, v90
	v_cvt_f32_i32_e32 v91, v91
	v_cvt_f32_i32_e32 v92, v92
	v_cvt_f32_i32_e32 v93, v93
	v_cvt_f32_i32_e32 v86, v86
	v_cvt_f32_i32_e32 v87, v87
	v_cvt_f32_i32_e32 v88, v88
	v_cvt_f32_i32_e32 v89, v89
	v_cvt_f32_i32_e32 v74, v74
	v_cvt_f32_i32_e32 v75, v75
	v_cvt_f32_i32_e32 v76, v76
	v_cvt_f32_i32_e32 v77, v77
	v_cvt_f32_i32_e32 v114, v114
	v_cvt_f32_i32_e32 v115, v115
	v_cvt_f32_i32_e32 v116, v116
	v_cvt_f32_i32_e32 v117, v117
	v_cvt_f32_i32_e32 v110, v110
	v_cvt_f32_i32_e32 v111, v111
	v_cvt_f32_i32_e32 v112, v112
	v_cvt_f32_i32_e32 v113, v113
	v_cvt_f32_i32_e32 v98, v98
	v_cvt_f32_i32_e32 v99, v99
	v_cvt_f32_i32_e32 v100, v100
	v_cvt_f32_i32_e32 v101, v101
	v_cvt_f32_i32_e32 v94, v94
	v_cvt_f32_i32_e32 v95, v95
	v_cvt_f32_i32_e32 v96, v96
	v_cvt_f32_i32_e32 v97, v97
	v_cvt_f32_i32_e32 v82, v82
	v_cvt_f32_i32_e32 v83, v83
	v_cvt_f32_i32_e32 v84, v84
	v_cvt_f32_i32_e32 v85, v85
	v_cvt_f32_i32_e32 v78, v78
	v_cvt_f32_i32_e32 v79, v79
	v_cvt_f32_i32_e32 v80, v80
	v_cvt_f32_i32_e32 v81, v81
	v_cvt_f32_i32_e32 v70, v70
	v_cvt_f32_i32_e32 v71, v71
	v_cvt_f32_i32_e32 v72, v72
	v_cvt_f32_i32_e32 v73, v73
	v_cvt_f32_i32_e32 v66, v66
	v_cvt_f32_i32_e32 v67, v67
	v_cvt_f32_i32_e32 v68, v68
	v_cvt_f32_i32_e32 v69, v69
	v_cvt_f32_i32_e32 v62, v62
	v_cvt_f32_i32_e32 v63, v63
	v_cvt_f32_i32_e32 v64, v64
	v_cvt_f32_i32_e32 v65, v65
	v_cvt_f32_i32_e32 v58, v58
	v_cvt_f32_i32_e32 v59, v59
	v_cvt_f32_i32_e32 v60, v60
	v_cvt_f32_i32_e32 v61, v61
	v_cvt_f32_i32_e32 v46, v46
	v_cvt_f32_i32_e32 v47, v47
	v_cvt_f32_i32_e32 v48, v48
	v_cvt_f32_i32_e32 v49, v49
	v_cvt_f32_i32_e32 v42, v42
	v_cvt_f32_i32_e32 v43, v43
	v_cvt_f32_i32_e32 v44, v44
	v_cvt_f32_i32_e32 v45, v45
	v_cvt_f32_i32_e32 v38, v38
	v_cvt_f32_i32_e32 v39, v39
	v_cvt_f32_i32_e32 v40, v40
	v_cvt_f32_i32_e32 v41, v41
	v_cvt_f32_i32_e32 v34, v34
	v_cvt_f32_i32_e32 v35, v35
	v_cvt_f32_i32_e32 v36, v36
	v_cvt_f32_i32_e32 v37, v37
	v_cvt_f32_i32_e32 v22, v22
	v_cvt_f32_i32_e32 v23, v23
	v_cvt_f32_i32_e32 v24, v24
	v_cvt_f32_i32_e32 v25, v25
	v_cvt_f32_i32_e32 v18, v18
	v_cvt_f32_i32_e32 v19, v19
	v_cvt_f32_i32_e32 v20, v20
	v_cvt_f32_i32_e32 v21, v21
	v_cvt_f32_i32_e32 v54, v54
	v_cvt_f32_i32_e32 v55, v55
	v_cvt_f32_i32_e32 v56, v56
	v_cvt_f32_i32_e32 v57, v57
	v_cvt_f32_i32_e32 v50, v50
	v_cvt_f32_i32_e32 v51, v51
	v_cvt_f32_i32_e32 v52, v52
	v_cvt_f32_i32_e32 v53, v53
	v_cvt_f32_i32_e32 v30, v30
	v_cvt_f32_i32_e32 v31, v31
	v_cvt_f32_i32_e32 v32, v32
	v_cvt_f32_i32_e32 v33, v33
	v_cvt_f32_i32_e32 v26, v26
	v_cvt_f32_i32_e32 v27, v27
	v_cvt_f32_i32_e32 v28, v28
	v_cvt_f32_i32_e32 v29, v29
	v_cvt_f32_i32_e32 v14, v14
	v_cvt_f32_i32_e32 v15, v15
	v_cvt_f32_i32_e32 v16, v16
	v_cvt_f32_i32_e32 v17, v17
	v_cvt_f32_i32_e32 v10, v10
	v_cvt_f32_i32_e32 v11, v11
	v_cvt_f32_i32_e32 v12, v12
	v_cvt_f32_i32_e32 v13, v13
	v_cvt_f32_i32_e32 v6, v6
	v_cvt_f32_i32_e32 v7, v7
	v_cvt_f32_i32_e32 v8, v8
	v_cvt_f32_i32_e32 v9, v9
	v_cvt_f32_i32_e32 v2, v2
	v_cvt_f32_i32_e32 v3, v3
	v_cvt_f32_i32_e32 v4, v4
	v_cvt_f32_i32_e32 v5, v5
	s_waitcnt lgkmcnt(0)
	v_mul_f32_e32 v194, 0x3a4d4011, v194
	v_mul_f32_e32 v196, 0x3a4d4011, v196
	v_mul_f32_e32 v198, 0x3a4d4011, v198
	v_mul_f32_e32 v200, 0x3a4d4011, v200
	v_mul_f32_e32 v202, 0x3a4d4011, v202
	v_mul_f32_e32 v204, 0x3a4d4011, v204
	v_mul_f32_e32 v206, 0x3a4d4011, v206
	v_mul_f32_e32 v208, 0x3a4d4011, v208
	s_waitcnt vmcnt(0)
;     __device__ __forceinline__ void operator()(const f32x4 (&acc)[2][2][4][2], const Unit& u, int wr, int wc, int fr, int fq) const {
;     ...
;                     const f32x4 gt = acc[ai][0][m][n] * descale + (n ? g1 : g0), up = acc[ai][1][m][n] * descale + (n ? u1 : u0);
; #pragma unroll
;                     for (int j = 0; j < 4; ++j) { const float g = fminf(gt[j], 7.0f), uu = fminf(fmaxf(up[j], -7.0f), 7.0f);
;                         const float sg = __builtin_amdgcn_rcpf(1.0f + __builtin_amdgcn_exp2f(g * (-1.702f * 1.4426950408889634f)));
;                         o[n][j] = (uu + 1.0f) * (g * sg) * oscale; }
;                 }
;                 w0[m] = __builtin_amdgcn_cvt_pk_fp8_f32(o[0][0], o[0][1], 0, false); w0[m] = __builtin_amdgcn_cvt_pk_fp8_f32(o[0][2], o[0][3], w0[m], true);
	v_pk_fma_f32 v[126:127], v[126:127], v[194:195], v[132:133] op_sel_hi:[1,0,1]
	v_pk_fma_f32 v[128:129], v[128:129], v[194:195], v[134:135] op_sel_hi:[1,0,1]
	v_pk_fma_f32 v[122:123], v[122:123], v[194:195], v[136:137] op_sel_hi:[1,0,1]
	v_pk_fma_f32 v[124:125], v[124:125], v[194:195], v[138:139] op_sel_hi:[1,0,1]
	v_pk_fma_f32 v[118:119], v[118:119], v[196:197], v[132:133] op_sel_hi:[1,0,1]
	v_pk_fma_f32 v[120:121], v[120:121], v[196:197], v[134:135] op_sel_hi:[1,0,1]
	v_pk_fma_f32 v[106:107], v[106:107], v[196:197], v[136:137] op_sel_hi:[1,0,1]
	v_pk_fma_f32 v[108:109], v[108:109], v[196:197], v[138:139] op_sel_hi:[1,0,1]
	v_pk_fma_f32 v[114:115], v[114:115], v[194:195], v[140:141] op_sel_hi:[1,0,1]
	v_pk_fma_f32 v[116:117], v[116:117], v[194:195], v[142:143] op_sel_hi:[1,0,1]
	v_pk_fma_f32 v[110:111], v[110:111], v[194:195], v[144:145] op_sel_hi:[1,0,1]
	v_pk_fma_f32 v[112:113], v[112:113], v[194:195], v[146:147] op_sel_hi:[1,0,1]
	v_pk_fma_f32 v[98:99], v[98:99], v[196:197], v[140:141] op_sel_hi:[1,0,1]
	v_pk_fma_f32 v[100:101], v[100:101], v[196:197], v[142:143] op_sel_hi:[1,0,1]
	v_pk_fma_f32 v[94:95], v[94:95], v[196:197], v[144:145] op_sel_hi:[1,0,1]
	v_pk_fma_f32 v[96:97], v[96:97], v[196:197], v[146:147] op_sel_hi:[1,0,1]
	v_min_f32_e32 v126, 0x40e00000, v126
	v_min_f32_e32 v127, 0x40e00000, v127
	v_min_f32_e32 v128, 0x40e00000, v128
	v_min_f32_e32 v129, 0x40e00000, v129
	v_min_f32_e32 v122, 0x40e00000, v122
	v_min_f32_e32 v123, 0x40e00000, v123
	v_min_f32_e32 v124, 0x40e00000, v124
	v_min_f32_e32 v125, 0x40e00000, v125
	v_min_f32_e32 v118, 0x40e00000, v118
	v_min_f32_e32 v119, 0x40e00000, v119
	v_min_f32_e32 v120, 0x40e00000, v120
	v_min_f32_e32 v121, 0x40e00000, v121
	v_min_f32_e32 v106, 0x40e00000, v106
	v_min_f32_e32 v107, 0x40e00000, v107
	v_min_f32_e32 v108, 0x40e00000, v108
	v_min_f32_e32 v109, 0x40e00000, v109
	v_pk_mul_f32 v[210:211], v[126:127], s[98:99] op_sel_hi:[1,0]
	v_pk_mul_f32 v[212:213], v[128:129], s[98:99] op_sel_hi:[1,0]
	v_pk_mul_f32 v[214:215], v[122:123], s[98:99] op_sel_hi:[1,0]
	v_pk_mul_f32 v[216:217], v[124:125], s[98:99] op_sel_hi:[1,0]
	v_pk_mul_f32 v[218:219], v[118:119], s[98:99] op_sel_hi:[1,0]
	v_pk_mul_f32 v[220:221], v[120:121], s[98:99] op_sel_hi:[1,0]
	v_pk_mul_f32 v[222:223], v[106:107], s[98:99] op_sel_hi:[1,0]
	v_pk_mul_f32 v[224:225], v[108:109], s[98:99] op_sel_hi:[1,0]
	v_exp_f32_e32 v210, v210
	v_exp_f32_e32 v211, v211
	v_exp_f32_e32 v212, v212
	v_exp_f32_e32 v213, v213
	v_exp_f32_e32 v214, v214
	v_exp_f32_e32 v215, v215
	v_exp_f32_e32 v216, v216
	v_exp_f32_e32 v217, v217
	v_exp_f32_e32 v218, v218
	v_exp_f32_e32 v219, v219
	v_exp_f32_e32 v220, v220
	v_exp_f32_e32 v221, v221
	v_exp_f32_e32 v222, v222
	v_exp_f32_e32 v223, v223
	v_exp_f32_e32 v224, v224
	v_exp_f32_e32 v225, v225
	v_med3_f32 v114, v114, s65, v183
	v_med3_f32 v115, v115, s65, v183
	v_med3_f32 v116, v116, s65, v183
	v_med3_f32 v117, v117, s65, v183
	v_med3_f32 v110, v110, s65, v183
	v_med3_f32 v111, v111, s65, v183
	v_med3_f32 v112, v112, s65, v183
	v_med3_f32 v113, v113, s65, v183
	v_med3_f32 v98, v98, s65, v183
	v_med3_f32 v99, v99, s65, v183
	v_med3_f32 v100, v100, s65, v183
	v_med3_f32 v101, v101, s65, v183
	v_med3_f32 v94, v94, s65, v183
	v_med3_f32 v95, v95, s65, v183
	v_med3_f32 v96, v96, s65, v183
	v_med3_f32 v97, v97, s65, v183
	v_pk_add_f32 v[210:211], v[210:211], 1.0 op_sel_hi:[1,0]
	v_pk_add_f32 v[212:213], v[212:213], 1.0 op_sel_hi:[1,0]
	v_pk_add_f32 v[214:215], v[214:215], 1.0 op_sel_hi:[1,0]
	v_pk_add_f32 v[216:217], v[216:217], 1.0 op_sel_hi:[1,0]
	v_pk_add_f32 v[218:219], v[218:219], 1.0 op_sel_hi:[1,0]
	v_pk_add_f32 v[220:221], v[220:221], 1.0 op_sel_hi:[1,0]
	v_pk_add_f32 v[222:223], v[222:223], 1.0 op_sel_hi:[1,0]
	v_pk_add_f32 v[224:225], v[224:225], 1.0 op_sel_hi:[1,0]
	v_rcp_f32_e32 v210, v210
	v_rcp_f32_e32 v211, v211
	v_rcp_f32_e32 v212, v212
	v_rcp_f32_e32 v213, v213
	v_rcp_f32_e32 v214, v214
	v_rcp_f32_e32 v215, v215
	v_rcp_f32_e32 v216, v216
	v_rcp_f32_e32 v217, v217
	v_rcp_f32_e32 v218, v218
	v_rcp_f32_e32 v219, v219
	v_rcp_f32_e32 v220, v220
	v_rcp_f32_e32 v221, v221
	v_rcp_f32_e32 v222, v222
	v_rcp_f32_e32 v223, v223
	v_rcp_f32_e32 v224, v224
	v_rcp_f32_e32 v225, v225
	v_pk_fma_f32 v[114:115], v[114:115], 4.0, 4.0 op_sel_hi:[1,0,0]
	v_pk_fma_f32 v[116:117], v[116:117], 4.0, 4.0 op_sel_hi:[1,0,0]
	v_pk_fma_f32 v[110:111], v[110:111], 4.0, 4.0 op_sel_hi:[1,0,0]
	v_pk_fma_f32 v[112:113], v[112:113], 4.0, 4.0 op_sel_hi:[1,0,0]
	v_pk_fma_f32 v[98:99], v[98:99], 4.0, 4.0 op_sel_hi:[1,0,0]
	v_pk_fma_f32 v[100:101], v[100:101], 4.0, 4.0 op_sel_hi:[1,0,0]
	v_pk_fma_f32 v[94:95], v[94:95], 4.0, 4.0 op_sel_hi:[1,0,0]
	v_pk_fma_f32 v[96:97], v[96:97], 4.0, 4.0 op_sel_hi:[1,0,0]
	v_pk_mul_f32 v[126:127], v[126:127], v[210:211]
	v_pk_mul_f32 v[128:129], v[128:129], v[212:213]
	v_pk_mul_f32 v[122:123], v[122:123], v[214:215]
	v_pk_mul_f32 v[124:125], v[124:125], v[216:217]
	v_pk_mul_f32 v[118:119], v[118:119], v[218:219]
	v_pk_mul_f32 v[120:121], v[120:121], v[220:221]
	v_pk_mul_f32 v[106:107], v[106:107], v[222:223]
	v_pk_mul_f32 v[108:109], v[108:109], v[224:225]
	v_pk_mul_f32 v[126:127], v[126:127], v[114:115]
	v_pk_mul_f32 v[128:129], v[128:129], v[116:117]
	v_pk_mul_f32 v[122:123], v[122:123], v[110:111]
	v_pk_mul_f32 v[124:125], v[124:125], v[112:113]
	v_pk_mul_f32 v[118:119], v[118:119], v[98:99]
	v_pk_mul_f32 v[120:121], v[120:121], v[100:101]
	v_pk_mul_f32 v[106:107], v[106:107], v[94:95]
	v_pk_mul_f32 v[108:109], v[108:109], v[96:97]
	v_cvt_pk_fp8_f32 v226, v126, v127
	v_cvt_pk_fp8_f32 v226, v128, v129 op_sel:[0,0,1]
	v_cvt_pk_fp8_f32 v227, v122, v123
	v_cvt_pk_fp8_f32 v227, v124, v125 op_sel:[0,0,1]
; __device__ __forceinline__ void swap16(int& x, int& y) { const auto r = __builtin_amdgcn_permlane16_swap((unsigned)x, (unsigned)y, false, false); x = (int)r[0]; y = (int)r[1]; }
;     __device__ __forceinline__ void operator()(const f32x4 (&acc)[2][2][4][2], const Unit& u, int wr, int wc, int fr, int fq) const {
;     ...
;                     const f32x4 gt = acc[ai][0][m][n] * descale + (n ? g1 : g0), up = acc[ai][1][m][n] * descale + (n ? u1 : u0);
; #pragma unroll
;                     for (int j = 0; j < 4; ++j) { const float g = fminf(gt[j], 7.0f), uu = fminf(fmaxf(up[j], -7.0f), 7.0f);
;                         const float sg = __builtin_amdgcn_rcpf(1.0f + __builtin_amdgcn_exp2f(g * (-1.702f * 1.4426950408889634f)));
;                         o[n][j] = (uu + 1.0f) * (g * sg) * oscale; }
;     ...
;                 w0[m] = __builtin_amdgcn_cvt_pk_fp8_f32(o[0][0], o[0][1], 0, false); w0[m] = __builtin_amdgcn_cvt_pk_fp8_f32(o[0][2], o[0][3], w0[m], true);
;                 w1[m] = __builtin_amdgcn_cvt_pk_fp8_f32(o[1][0], o[1][1], 0, false); w1[m] = __builtin_amdgcn_cvt_pk_fp8_f32(o[1][2], o[1][3], w1[m], true);
;             }
; #pragma unroll
;             for (int p = 0; p < 2; ++p) { swap16(w0[2 * p], w0[2 * p + 1]); swap16(w1[2 * p], w1[2 * p + 1]);
;                 u32x4 w; w.x = (unsigned)w0[2 * p]; w.y = (unsigned)w1[2 * p]; w.z = (unsigned)w0[2 * p + 1]; w.w = (unsigned)w1[2 * p + 1];
;                 *(u32x4*)(ACT + (size_t)(row0 + ai * HALF + (2 * p + odd) * 16) * DFF + colw) = w; }
	v_cvt_pk_fp8_f32 v228, v118, v119
	v_cvt_pk_fp8_f32 v228, v120, v121 op_sel:[0,0,1]
	v_cvt_pk_fp8_f32 v229, v106, v107
	v_cvt_pk_fp8_f32 v229, v108, v109 op_sel:[0,0,1]
	v_or_b32_e32 v230, v232, v172
	v_ashrrev_i32_e32 v231, 31, v230
	v_lshlrev_b64 v[230:231], 11, v[230:231]
	v_permlane16_swap_b32_e32 v226, v228
	v_permlane16_swap_b32_e32 v227, v229
	v_lshl_add_u64 v[230:231], s[16:17], 0, v[230:231]
	v_lshl_add_u64 v[230:231], v[230:231], 0, v[234:235]
	global_store_dwordx4 v[230:231], v[226:229], off
	v_pk_fma_f32 v[102:103], v[102:103], v[198:199], v[132:133] op_sel_hi:[1,0,1]
	v_pk_fma_f32 v[104:105], v[104:105], v[198:199], v[134:135] op_sel_hi:[1,0,1]
	v_pk_fma_f32 v[90:91], v[90:91], v[198:199], v[136:137] op_sel_hi:[1,0,1]
	v_pk_fma_f32 v[92:93], v[92:93], v[198:199], v[138:139] op_sel_hi:[1,0,1]
	v_pk_fma_f32 v[86:87], v[86:87], v[200:201], v[132:133] op_sel_hi:[1,0,1]
	v_pk_fma_f32 v[88:89], v[88:89], v[200:201], v[134:135] op_sel_hi:[1,0,1]
	v_pk_fma_f32 v[74:75], v[74:75], v[200:201], v[136:137] op_sel_hi:[1,0,1]
	v_pk_fma_f32 v[76:77], v[76:77], v[200:201], v[138:139] op_sel_hi:[1,0,1]
	v_pk_fma_f32 v[82:83], v[82:83], v[198:199], v[140:141] op_sel_hi:[1,0,1]
	v_pk_fma_f32 v[84:85], v[84:85], v[198:199], v[142:143] op_sel_hi:[1,0,1]
	v_pk_fma_f32 v[78:79], v[78:79], v[198:199], v[144:145] op_sel_hi:[1,0,1]
	v_pk_fma_f32 v[80:81], v[80:81], v[198:199], v[146:147] op_sel_hi:[1,0,1]
	v_pk_fma_f32 v[70:71], v[70:71], v[200:201], v[140:141] op_sel_hi:[1,0,1]
	v_pk_fma_f32 v[72:73], v[72:73], v[200:201], v[142:143] op_sel_hi:[1,0,1]
	v_pk_fma_f32 v[66:67], v[66:67], v[200:201], v[144:145] op_sel_hi:[1,0,1]
	v_pk_fma_f32 v[68:69], v[68:69], v[200:201], v[146:147] op_sel_hi:[1,0,1]
	v_min_f32_e32 v102, 0x40e00000, v102
	v_min_f32_e32 v103, 0x40e00000, v103
	v_min_f32_e32 v104, 0x40e00000, v104
	v_min_f32_e32 v105, 0x40e00000, v105
	v_min_f32_e32 v90, 0x40e00000, v90
	v_min_f32_e32 v91, 0x40e00000, v91
	v_min_f32_e32 v92, 0x40e00000, v92
	v_min_f32_e32 v93, 0x40e00000, v93
	v_min_f32_e32 v86, 0x40e00000, v86
	v_min_f32_e32 v87, 0x40e00000, v87
	v_min_f32_e32 v88, 0x40e00000, v88
	v_min_f32_e32 v89, 0x40e00000, v89
	v_min_f32_e32 v74, 0x40e00000, v74
	v_min_f32_e32 v75, 0x40e00000, v75
	v_min_f32_e32 v76, 0x40e00000, v76
	v_min_f32_e32 v77, 0x40e00000, v77
	v_pk_mul_f32 v[210:211], v[102:103], s[98:99] op_sel_hi:[1,0]
	v_pk_mul_f32 v[212:213], v[104:105], s[98:99] op_sel_hi:[1,0]
	v_pk_mul_f32 v[214:215], v[90:91], s[98:99] op_sel_hi:[1,0]
	v_pk_mul_f32 v[216:217], v[92:93], s[98:99] op_sel_hi:[1,0]
	v_pk_mul_f32 v[218:219], v[86:87], s[98:99] op_sel_hi:[1,0]
	v_pk_mul_f32 v[220:221], v[88:89], s[98:99] op_sel_hi:[1,0]
	v_pk_mul_f32 v[222:223], v[74:75], s[98:99] op_sel_hi:[1,0]
	v_pk_mul_f32 v[224:225], v[76:77], s[98:99] op_sel_hi:[1,0]
	v_exp_f32_e32 v210, v210
	v_exp_f32_e32 v211, v211
	v_exp_f32_e32 v212, v212
	v_exp_f32_e32 v213, v213
	v_exp_f32_e32 v214, v214
	v_exp_f32_e32 v215, v215
	v_exp_f32_e32 v216, v216
	v_exp_f32_e32 v217, v217
	v_exp_f32_e32 v218, v218
	v_exp_f32_e32 v219, v219
	v_exp_f32_e32 v220, v220
	v_exp_f32_e32 v221, v221
	v_exp_f32_e32 v222, v222
	v_exp_f32_e32 v223, v223
	v_exp_f32_e32 v224, v224
	v_exp_f32_e32 v225, v225
	v_med3_f32 v82, v82, s65, v183
	v_med3_f32 v83, v83, s65, v183
	v_med3_f32 v84, v84, s65, v183
	v_med3_f32 v85, v85, s65, v183
	v_med3_f32 v78, v78, s65, v183
	v_med3_f32 v79, v79, s65, v183
	v_med3_f32 v80, v80, s65, v183
	v_med3_f32 v81, v81, s65, v183
	v_med3_f32 v70, v70, s65, v183
	v_med3_f32 v71, v71, s65, v183
	v_med3_f32 v72, v72, s65, v183
	v_med3_f32 v73, v73, s65, v183
	v_med3_f32 v66, v66, s65, v183
	v_med3_f32 v67, v67, s65, v183
	v_med3_f32 v68, v68, s65, v183
	v_med3_f32 v69, v69, s65, v183
	v_pk_add_f32 v[210:211], v[210:211], 1.0 op_sel_hi:[1,0]
	v_pk_add_f32 v[212:213], v[212:213], 1.0 op_sel_hi:[1,0]
	v_pk_add_f32 v[214:215], v[214:215], 1.0 op_sel_hi:[1,0]
	v_pk_add_f32 v[216:217], v[216:217], 1.0 op_sel_hi:[1,0]
	v_pk_add_f32 v[218:219], v[218:219], 1.0 op_sel_hi:[1,0]
	v_pk_add_f32 v[220:221], v[220:221], 1.0 op_sel_hi:[1,0]
	v_pk_add_f32 v[222:223], v[222:223], 1.0 op_sel_hi:[1,0]
	v_pk_add_f32 v[224:225], v[224:225], 1.0 op_sel_hi:[1,0]
	v_rcp_f32_e32 v210, v210
	v_rcp_f32_e32 v211, v211
	v_rcp_f32_e32 v212, v212
	v_rcp_f32_e32 v213, v213
	v_rcp_f32_e32 v214, v214
	v_rcp_f32_e32 v215, v215
	v_rcp_f32_e32 v216, v216
	v_rcp_f32_e32 v217, v217
	v_rcp_f32_e32 v218, v218
	v_rcp_f32_e32 v219, v219
	v_rcp_f32_e32 v220, v220
	v_rcp_f32_e32 v221, v221
	v_rcp_f32_e32 v222, v222
	v_rcp_f32_e32 v223, v223
	v_rcp_f32_e32 v224, v224
	v_rcp_f32_e32 v225, v225
	v_pk_fma_f32 v[82:83], v[82:83], 4.0, 4.0 op_sel_hi:[1,0,0]
	v_pk_fma_f32 v[84:85], v[84:85], 4.0, 4.0 op_sel_hi:[1,0,0]
	v_pk_fma_f32 v[78:79], v[78:79], 4.0, 4.0 op_sel_hi:[1,0,0]
	v_pk_fma_f32 v[80:81], v[80:81], 4.0, 4.0 op_sel_hi:[1,0,0]
	v_pk_fma_f32 v[70:71], v[70:71], 4.0, 4.0 op_sel_hi:[1,0,0]
	v_pk_fma_f32 v[72:73], v[72:73], 4.0, 4.0 op_sel_hi:[1,0,0]
	v_pk_fma_f32 v[66:67], v[66:67], 4.0, 4.0 op_sel_hi:[1,0,0]
	v_pk_fma_f32 v[68:69], v[68:69], 4.0, 4.0 op_sel_hi:[1,0,0]
	v_pk_mul_f32 v[102:103], v[102:103], v[210:211]
	v_pk_mul_f32 v[104:105], v[104:105], v[212:213]
	v_pk_mul_f32 v[90:91], v[90:91], v[214:215]
	v_pk_mul_f32 v[92:93], v[92:93], v[216:217]
	v_pk_mul_f32 v[86:87], v[86:87], v[218:219]
	v_pk_mul_f32 v[88:89], v[88:89], v[220:221]
	v_pk_mul_f32 v[74:75], v[74:75], v[222:223]
	v_pk_mul_f32 v[76:77], v[76:77], v[224:225]
	v_pk_mul_f32 v[102:103], v[102:103], v[82:83]
	v_pk_mul_f32 v[104:105], v[104:105], v[84:85]
	v_pk_mul_f32 v[90:91], v[90:91], v[78:79]
	v_pk_mul_f32 v[92:93], v[92:93], v[80:81]
; __device__ __forceinline__ void swap16(int& x, int& y) { const auto r = __builtin_amdgcn_permlane16_swap((unsigned)x, (unsigned)y, false, false); x = (int)r[0]; y = (int)r[1]; }
;     __device__ __forceinline__ void operator()(const f32x4 (&acc)[2][2][4][2], const Unit& u, int wr, int wc, int fr, int fq) const {
;     ...
;                     const f32x4 gt = acc[ai][0][m][n] * descale + (n ? g1 : g0), up = acc[ai][1][m][n] * descale + (n ? u1 : u0);
; #pragma unroll
;                     for (int j = 0; j < 4; ++j) { const float g = fminf(gt[j], 7.0f), uu = fminf(fmaxf(up[j], -7.0f), 7.0f);
;                         const float sg = __builtin_amdgcn_rcpf(1.0f + __builtin_amdgcn_exp2f(g * (-1.702f * 1.4426950408889634f)));
;                         o[n][j] = (uu + 1.0f) * (g * sg) * oscale; }
;     ...
;                 w0[m] = __builtin_amdgcn_cvt_pk_fp8_f32(o[0][0], o[0][1], 0, false); w0[m] = __builtin_amdgcn_cvt_pk_fp8_f32(o[0][2], o[0][3], w0[m], true);
;                 w1[m] = __builtin_amdgcn_cvt_pk_fp8_f32(o[1][0], o[1][1], 0, false); w1[m] = __builtin_amdgcn_cvt_pk_fp8_f32(o[1][2], o[1][3], w1[m], true);
;             }
; #pragma unroll
;             for (int p = 0; p < 2; ++p) { swap16(w0[2 * p], w0[2 * p + 1]); swap16(w1[2 * p], w1[2 * p + 1]);
;                 u32x4 w; w.x = (unsigned)w0[2 * p]; w.y = (unsigned)w1[2 * p]; w.z = (unsigned)w0[2 * p + 1]; w.w = (unsigned)w1[2 * p + 1];
;                 *(u32x4*)(ACT + (size_t)(row0 + ai * HALF + (2 * p + odd) * 16) * DFF + colw) = w; }
	v_pk_mul_f32 v[86:87], v[86:87], v[70:71]
	v_pk_mul_f32 v[88:89], v[88:89], v[72:73]
	v_pk_mul_f32 v[74:75], v[74:75], v[66:67]
	v_pk_mul_f32 v[76:77], v[76:77], v[68:69]
	v_cvt_pk_fp8_f32 v236, v102, v103
	v_cvt_pk_fp8_f32 v236, v104, v105 op_sel:[0,0,1]
	v_cvt_pk_fp8_f32 v237, v90, v91
	v_cvt_pk_fp8_f32 v237, v92, v93 op_sel:[0,0,1]
	v_cvt_pk_fp8_f32 v238, v86, v87
	v_cvt_pk_fp8_f32 v238, v88, v89 op_sel:[0,0,1]
	v_cvt_pk_fp8_f32 v239, v74, v75
	v_cvt_pk_fp8_f32 v239, v76, v77 op_sel:[0,0,1]
	v_or_b32_e32 v230, v232, v173
	v_ashrrev_i32_e32 v231, 31, v230
	v_lshlrev_b64 v[230:231], 11, v[230:231]
	v_permlane16_swap_b32_e32 v236, v238
	v_permlane16_swap_b32_e32 v237, v239
	v_lshl_add_u64 v[230:231], s[16:17], 0, v[230:231]
	v_lshl_add_u64 v[230:231], v[230:231], 0, v[234:235]
	global_store_dwordx4 v[230:231], v[236:239], off
	v_pk_fma_f32 v[62:63], v[62:63], v[202:203], v[132:133] op_sel_hi:[1,0,1]
	v_pk_fma_f32 v[64:65], v[64:65], v[202:203], v[134:135] op_sel_hi:[1,0,1]
	v_pk_fma_f32 v[58:59], v[58:59], v[202:203], v[136:137] op_sel_hi:[1,0,1]
	v_pk_fma_f32 v[60:61], v[60:61], v[202:203], v[138:139] op_sel_hi:[1,0,1]
	v_pk_fma_f32 v[46:47], v[46:47], v[204:205], v[132:133] op_sel_hi:[1,0,1]
	v_pk_fma_f32 v[48:49], v[48:49], v[204:205], v[134:135] op_sel_hi:[1,0,1]
	v_pk_fma_f32 v[42:43], v[42:43], v[204:205], v[136:137] op_sel_hi:[1,0,1]
	v_pk_fma_f32 v[44:45], v[44:45], v[204:205], v[138:139] op_sel_hi:[1,0,1]
	v_pk_fma_f32 v[54:55], v[54:55], v[202:203], v[140:141] op_sel_hi:[1,0,1]
	v_pk_fma_f32 v[56:57], v[56:57], v[202:203], v[142:143] op_sel_hi:[1,0,1]
	v_pk_fma_f32 v[50:51], v[50:51], v[202:203], v[144:145] op_sel_hi:[1,0,1]
	v_pk_fma_f32 v[52:53], v[52:53], v[202:203], v[146:147] op_sel_hi:[1,0,1]
	v_pk_fma_f32 v[30:31], v[30:31], v[204:205], v[140:141] op_sel_hi:[1,0,1]
	v_pk_fma_f32 v[32:33], v[32:33], v[204:205], v[142:143] op_sel_hi:[1,0,1]
	v_pk_fma_f32 v[26:27], v[26:27], v[204:205], v[144:145] op_sel_hi:[1,0,1]
	v_pk_fma_f32 v[28:29], v[28:29], v[204:205], v[146:147] op_sel_hi:[1,0,1]
	v_min_f32_e32 v62, 0x40e00000, v62
	v_min_f32_e32 v63, 0x40e00000, v63
	v_min_f32_e32 v64, 0x40e00000, v64
	v_min_f32_e32 v65, 0x40e00000, v65
	v_min_f32_e32 v58, 0x40e00000, v58
	v_min_f32_e32 v59, 0x40e00000, v59
	v_min_f32_e32 v60, 0x40e00000, v60
	v_min_f32_e32 v61, 0x40e00000, v61
	v_min_f32_e32 v46, 0x40e00000, v46
	v_min_f32_e32 v47, 0x40e00000, v47
	v_min_f32_e32 v48, 0x40e00000, v48
	v_min_f32_e32 v49, 0x40e00000, v49
	v_min_f32_e32 v42, 0x40e00000, v42
	v_min_f32_e32 v43, 0x40e00000, v43
	v_min_f32_e32 v44, 0x40e00000, v44
	v_min_f32_e32 v45, 0x40e00000, v45
	v_pk_mul_f32 v[210:211], v[62:63], s[98:99] op_sel_hi:[1,0]
	v_pk_mul_f32 v[212:213], v[64:65], s[98:99] op_sel_hi:[1,0]
	v_pk_mul_f32 v[214:215], v[58:59], s[98:99] op_sel_hi:[1,0]
	v_pk_mul_f32 v[216:217], v[60:61], s[98:99] op_sel_hi:[1,0]
	v_pk_mul_f32 v[218:219], v[46:47], s[98:99] op_sel_hi:[1,0]
	v_pk_mul_f32 v[220:221], v[48:49], s[98:99] op_sel_hi:[1,0]
	v_pk_mul_f32 v[222:223], v[42:43], s[98:99] op_sel_hi:[1,0]
	v_pk_mul_f32 v[224:225], v[44:45], s[98:99] op_sel_hi:[1,0]
	v_exp_f32_e32 v210, v210
	v_exp_f32_e32 v211, v211
	v_exp_f32_e32 v212, v212
	v_exp_f32_e32 v213, v213
	v_exp_f32_e32 v214, v214
	v_exp_f32_e32 v215, v215
	v_exp_f32_e32 v216, v216
	v_exp_f32_e32 v217, v217
	v_exp_f32_e32 v218, v218
	v_exp_f32_e32 v219, v219
	v_exp_f32_e32 v220, v220
	v_exp_f32_e32 v221, v221
	v_exp_f32_e32 v222, v222
	v_exp_f32_e32 v223, v223
	v_exp_f32_e32 v224, v224
	v_exp_f32_e32 v225, v225
	v_med3_f32 v54, v54, s65, v183
	v_med3_f32 v55, v55, s65, v183
	v_med3_f32 v56, v56, s65, v183
	v_med3_f32 v57, v57, s65, v183
	v_med3_f32 v50, v50, s65, v183
	v_med3_f32 v51, v51, s65, v183
	v_med3_f32 v52, v52, s65, v183
	v_med3_f32 v53, v53, s65, v183
	v_med3_f32 v30, v30, s65, v183
	v_med3_f32 v31, v31, s65, v183
	v_med3_f32 v32, v32, s65, v183
	v_med3_f32 v33, v33, s65, v183
	v_med3_f32 v26, v26, s65, v183
	v_med3_f32 v27, v27, s65, v183
	v_med3_f32 v28, v28, s65, v183
	v_med3_f32 v29, v29, s65, v183
	v_pk_add_f32 v[210:211], v[210:211], 1.0 op_sel_hi:[1,0]
	v_pk_add_f32 v[212:213], v[212:213], 1.0 op_sel_hi:[1,0]
	v_pk_add_f32 v[214:215], v[214:215], 1.0 op_sel_hi:[1,0]
	v_pk_add_f32 v[216:217], v[216:217], 1.0 op_sel_hi:[1,0]
	v_pk_add_f32 v[218:219], v[218:219], 1.0 op_sel_hi:[1,0]
	v_pk_add_f32 v[220:221], v[220:221], 1.0 op_sel_hi:[1,0]
	v_pk_add_f32 v[222:223], v[222:223], 1.0 op_sel_hi:[1,0]
	v_pk_add_f32 v[224:225], v[224:225], 1.0 op_sel_hi:[1,0]
	v_rcp_f32_e32 v210, v210
	v_rcp_f32_e32 v211, v211
	v_rcp_f32_e32 v212, v212
	v_rcp_f32_e32 v213, v213
	v_rcp_f32_e32 v214, v214
	v_rcp_f32_e32 v215, v215
	v_rcp_f32_e32 v216, v216
	v_rcp_f32_e32 v217, v217
	v_rcp_f32_e32 v218, v218
	v_rcp_f32_e32 v219, v219
	v_rcp_f32_e32 v220, v220
	v_rcp_f32_e32 v221, v221
	v_rcp_f32_e32 v222, v222
	v_rcp_f32_e32 v223, v223
	v_rcp_f32_e32 v224, v224
	v_rcp_f32_e32 v225, v225
	v_pk_fma_f32 v[54:55], v[54:55], 4.0, 4.0 op_sel_hi:[1,0,0]
	v_pk_fma_f32 v[56:57], v[56:57], 4.0, 4.0 op_sel_hi:[1,0,0]
	v_pk_fma_f32 v[50:51], v[50:51], 4.0, 4.0 op_sel_hi:[1,0,0]
	v_pk_fma_f32 v[52:53], v[52:53], 4.0, 4.0 op_sel_hi:[1,0,0]
	v_pk_fma_f32 v[30:31], v[30:31], 4.0, 4.0 op_sel_hi:[1,0,0]
	v_pk_fma_f32 v[32:33], v[32:33], 4.0, 4.0 op_sel_hi:[1,0,0]
	v_pk_fma_f32 v[26:27], v[26:27], 4.0, 4.0 op_sel_hi:[1,0,0]
	v_pk_fma_f32 v[28:29], v[28:29], 4.0, 4.0 op_sel_hi:[1,0,0]
	v_pk_mul_f32 v[62:63], v[62:63], v[210:211]
	v_pk_mul_f32 v[64:65], v[64:65], v[212:213]
	v_pk_mul_f32 v[58:59], v[58:59], v[214:215]
	v_pk_mul_f32 v[60:61], v[60:61], v[216:217]
	v_pk_mul_f32 v[46:47], v[46:47], v[218:219]
; __device__ __forceinline__ void swap16(int& x, int& y) { const auto r = __builtin_amdgcn_permlane16_swap((unsigned)x, (unsigned)y, false, false); x = (int)r[0]; y = (int)r[1]; }
;     __device__ __forceinline__ void operator()(const f32x4 (&acc)[2][2][4][2], const Unit& u, int wr, int wc, int fr, int fq) const {
;     ...
;                     const f32x4 gt = acc[ai][0][m][n] * descale + (n ? g1 : g0), up = acc[ai][1][m][n] * descale + (n ? u1 : u0);
; #pragma unroll
;                     for (int j = 0; j < 4; ++j) { const float g = fminf(gt[j], 7.0f), uu = fminf(fmaxf(up[j], -7.0f), 7.0f);
;                         const float sg = __builtin_amdgcn_rcpf(1.0f + __builtin_amdgcn_exp2f(g * (-1.702f * 1.4426950408889634f)));
;                         o[n][j] = (uu + 1.0f) * (g * sg) * oscale; }
;     ...
;                 w0[m] = __builtin_amdgcn_cvt_pk_fp8_f32(o[0][0], o[0][1], 0, false); w0[m] = __builtin_amdgcn_cvt_pk_fp8_f32(o[0][2], o[0][3], w0[m], true);
;                 w1[m] = __builtin_amdgcn_cvt_pk_fp8_f32(o[1][0], o[1][1], 0, false); w1[m] = __builtin_amdgcn_cvt_pk_fp8_f32(o[1][2], o[1][3], w1[m], true);
;             }
; #pragma unroll
;             for (int p = 0; p < 2; ++p) { swap16(w0[2 * p], w0[2 * p + 1]); swap16(w1[2 * p], w1[2 * p + 1]);
;                 u32x4 w; w.x = (unsigned)w0[2 * p]; w.y = (unsigned)w1[2 * p]; w.z = (unsigned)w0[2 * p + 1]; w.w = (unsigned)w1[2 * p + 1];
;                 *(u32x4*)(ACT + (size_t)(row0 + ai * HALF + (2 * p + odd) * 16) * DFF + colw) = w; }
	v_pk_mul_f32 v[48:49], v[48:49], v[220:221]
	v_pk_mul_f32 v[42:43], v[42:43], v[222:223]
	v_pk_mul_f32 v[44:45], v[44:45], v[224:225]
	v_pk_mul_f32 v[62:63], v[62:63], v[54:55]
	v_pk_mul_f32 v[64:65], v[64:65], v[56:57]
	v_pk_mul_f32 v[58:59], v[58:59], v[50:51]
	v_pk_mul_f32 v[60:61], v[60:61], v[52:53]
	v_pk_mul_f32 v[46:47], v[46:47], v[30:31]
	v_pk_mul_f32 v[48:49], v[48:49], v[32:33]
	v_pk_mul_f32 v[42:43], v[42:43], v[26:27]
	v_pk_mul_f32 v[44:45], v[44:45], v[28:29]
	v_cvt_pk_fp8_f32 v240, v62, v63
	v_cvt_pk_fp8_f32 v240, v64, v65 op_sel:[0,0,1]
	v_cvt_pk_fp8_f32 v241, v58, v59
	v_cvt_pk_fp8_f32 v241, v60, v61 op_sel:[0,0,1]
	v_cvt_pk_fp8_f32 v242, v46, v47
	v_cvt_pk_fp8_f32 v242, v48, v49 op_sel:[0,0,1]
	v_cvt_pk_fp8_f32 v243, v42, v43
	v_cvt_pk_fp8_f32 v243, v44, v45 op_sel:[0,0,1]
	v_or_b32_e32 v230, v233, v172
	v_ashrrev_i32_e32 v231, 31, v230
	v_lshlrev_b64 v[230:231], 11, v[230:231]
	v_permlane16_swap_b32_e32 v240, v242
	v_permlane16_swap_b32_e32 v241, v243
	v_lshl_add_u64 v[230:231], s[16:17], 0, v[230:231]
	v_lshl_add_u64 v[230:231], v[230:231], 0, v[234:235]
	global_store_dwordx4 v[230:231], v[240:243], off
	v_pk_fma_f32 v[38:39], v[38:39], v[206:207], v[132:133] op_sel_hi:[1,0,1]
	v_pk_fma_f32 v[40:41], v[40:41], v[206:207], v[134:135] op_sel_hi:[1,0,1]
	v_pk_fma_f32 v[34:35], v[34:35], v[206:207], v[136:137] op_sel_hi:[1,0,1]
	v_pk_fma_f32 v[36:37], v[36:37], v[206:207], v[138:139] op_sel_hi:[1,0,1]
	v_pk_fma_f32 v[22:23], v[22:23], v[208:209], v[132:133] op_sel_hi:[1,0,1]
	v_pk_fma_f32 v[24:25], v[24:25], v[208:209], v[134:135] op_sel_hi:[1,0,1]
	v_pk_fma_f32 v[18:19], v[18:19], v[208:209], v[136:137] op_sel_hi:[1,0,1]
	v_pk_fma_f32 v[20:21], v[20:21], v[208:209], v[138:139] op_sel_hi:[1,0,1]
	v_pk_fma_f32 v[14:15], v[14:15], v[206:207], v[140:141] op_sel_hi:[1,0,1]
	v_pk_fma_f32 v[16:17], v[16:17], v[206:207], v[142:143] op_sel_hi:[1,0,1]
	v_pk_fma_f32 v[10:11], v[10:11], v[206:207], v[144:145] op_sel_hi:[1,0,1]
	v_pk_fma_f32 v[12:13], v[12:13], v[206:207], v[146:147] op_sel_hi:[1,0,1]
	v_pk_fma_f32 v[6:7], v[6:7], v[208:209], v[140:141] op_sel_hi:[1,0,1]
	v_pk_fma_f32 v[8:9], v[8:9], v[208:209], v[142:143] op_sel_hi:[1,0,1]
	v_pk_fma_f32 v[2:3], v[2:3], v[208:209], v[144:145] op_sel_hi:[1,0,1]
	v_pk_fma_f32 v[4:5], v[4:5], v[208:209], v[146:147] op_sel_hi:[1,0,1]
	v_min_f32_e32 v38, 0x40e00000, v38
	v_min_f32_e32 v39, 0x40e00000, v39
	v_min_f32_e32 v40, 0x40e00000, v40
	v_min_f32_e32 v41, 0x40e00000, v41
	v_min_f32_e32 v34, 0x40e00000, v34
	v_min_f32_e32 v35, 0x40e00000, v35
	v_min_f32_e32 v36, 0x40e00000, v36
	v_min_f32_e32 v37, 0x40e00000, v37
	v_min_f32_e32 v22, 0x40e00000, v22
	v_min_f32_e32 v23, 0x40e00000, v23
	v_min_f32_e32 v24, 0x40e00000, v24
	v_min_f32_e32 v25, 0x40e00000, v25
	v_min_f32_e32 v18, 0x40e00000, v18
	v_min_f32_e32 v19, 0x40e00000, v19
	v_min_f32_e32 v20, 0x40e00000, v20
	v_min_f32_e32 v21, 0x40e00000, v21
	v_pk_mul_f32 v[210:211], v[38:39], s[98:99] op_sel_hi:[1,0]
	v_pk_mul_f32 v[212:213], v[40:41], s[98:99] op_sel_hi:[1,0]
	v_pk_mul_f32 v[214:215], v[34:35], s[98:99] op_sel_hi:[1,0]
	v_pk_mul_f32 v[216:217], v[36:37], s[98:99] op_sel_hi:[1,0]
	v_pk_mul_f32 v[218:219], v[22:23], s[98:99] op_sel_hi:[1,0]
	v_pk_mul_f32 v[220:221], v[24:25], s[98:99] op_sel_hi:[1,0]
	v_pk_mul_f32 v[222:223], v[18:19], s[98:99] op_sel_hi:[1,0]
	v_pk_mul_f32 v[224:225], v[20:21], s[98:99] op_sel_hi:[1,0]
	v_exp_f32_e32 v210, v210
	v_exp_f32_e32 v211, v211
	v_exp_f32_e32 v212, v212
	v_exp_f32_e32 v213, v213
	v_exp_f32_e32 v214, v214
	v_exp_f32_e32 v215, v215
	v_exp_f32_e32 v216, v216
	v_exp_f32_e32 v217, v217
; __device__ __forceinline__ void swap16(int& x, int& y) { const auto r = __builtin_amdgcn_permlane16_swap((unsigned)x, (unsigned)y, false, false); x = (int)r[0]; y = (int)r[1]; }
; #define PG8_BAR __builtin_amdgcn_s_barrier()
;     __device__ __forceinline__ void operator()(const f32x4 (&acc)[2][2][4][2], const Unit& u, int wr, int wc, int fr, int fq) const {
;     ...
;                     const f32x4 gt = acc[ai][0][m][n] * descale + (n ? g1 : g0), up = acc[ai][1][m][n] * descale + (n ? u1 : u0);
; #pragma unroll
;                     for (int j = 0; j < 4; ++j) { const float g = fminf(gt[j], 7.0f), uu = fminf(fmaxf(up[j], -7.0f), 7.0f);
;                         const float sg = __builtin_amdgcn_rcpf(1.0f + __builtin_amdgcn_exp2f(g * (-1.702f * 1.4426950408889634f)));
;                         o[n][j] = (uu + 1.0f) * (g * sg) * oscale; }
;                 }
;                 w0[m] = __builtin_amdgcn_cvt_pk_fp8_f32(o[0][0], o[0][1], 0, false); w0[m] = __builtin_amdgcn_cvt_pk_fp8_f32(o[0][2], o[0][3], w0[m], true);
;                 w1[m] = __builtin_amdgcn_cvt_pk_fp8_f32(o[1][0], o[1][1], 0, false); w1[m] = __builtin_amdgcn_cvt_pk_fp8_f32(o[1][2], o[1][3], w1[m], true);
;             }
; #pragma unroll
;             for (int p = 0; p < 2; ++p) { swap16(w0[2 * p], w0[2 * p + 1]); swap16(w1[2 * p], w1[2 * p + 1]);
;                 u32x4 w; w.x = (unsigned)w0[2 * p]; w.y = (unsigned)w1[2 * p]; w.z = (unsigned)w0[2 * p + 1]; w.w = (unsigned)w1[2 * p + 1];
;                 *(u32x4*)(ACT + (size_t)(row0 + ai * HALF + (2 * p + odd) * 16) * DFF + colw) = w; }
; template <class Epi, bool GATHER, int MODE, bool SPLIT = false>
; __device__ __forceinline__ void gemm_phase(PG8_LAS unsigned char* lds, const Gemm g, const Order& S, const Epi& E) {
;     ...
;         if (!has_next) break;
; #pragma unroll
;         for (int a = 0; a < 2; ++a)
; #pragma unroll
;             for (int b = 0; b < 2; ++b)
; #pragma unroll
;                 for (int m = 0; m < 4; ++m)
; #pragma unroll
;                     for (int n = 0; n < 2; ++n) acc[a][b][m][n] = (f32x4){0.f, 0.f, 0.f, 0.f};
;         cur = nxt; cB = nB; cAr = nAr; ++ui;
; #pragma unroll
;         for (int h = 0; h < 2; ++h)
; #pragma unroll
;             for (int i = 0; i < 2; ++i) cv[h][i] = nv[h][i];
;         if (wr == 1) PG8_BAR;
	v_exp_f32_e32 v218, v218
	v_exp_f32_e32 v219, v219
	v_exp_f32_e32 v220, v220
	v_exp_f32_e32 v221, v221
	v_exp_f32_e32 v222, v222
	v_exp_f32_e32 v223, v223
	v_exp_f32_e32 v224, v224
	v_exp_f32_e32 v225, v225
	v_med3_f32 v14, v14, s65, v183
	v_med3_f32 v15, v15, s65, v183
	v_med3_f32 v16, v16, s65, v183
	v_med3_f32 v17, v17, s65, v183
	v_med3_f32 v10, v10, s65, v183
	v_med3_f32 v11, v11, s65, v183
	v_med3_f32 v12, v12, s65, v183
	v_med3_f32 v13, v13, s65, v183
	v_med3_f32 v6, v6, s65, v183
	v_med3_f32 v7, v7, s65, v183
	v_med3_f32 v8, v8, s65, v183
	v_med3_f32 v9, v9, s65, v183
	v_med3_f32 v2, v2, s65, v183
	v_med3_f32 v3, v3, s65, v183
	v_med3_f32 v4, v4, s65, v183
	v_med3_f32 v5, v5, s65, v183
	v_pk_add_f32 v[210:211], v[210:211], 1.0 op_sel_hi:[1,0]
	v_pk_add_f32 v[212:213], v[212:213], 1.0 op_sel_hi:[1,0]
	v_pk_add_f32 v[214:215], v[214:215], 1.0 op_sel_hi:[1,0]
	v_pk_add_f32 v[216:217], v[216:217], 1.0 op_sel_hi:[1,0]
	v_pk_add_f32 v[218:219], v[218:219], 1.0 op_sel_hi:[1,0]
	v_pk_add_f32 v[220:221], v[220:221], 1.0 op_sel_hi:[1,0]
	v_pk_add_f32 v[222:223], v[222:223], 1.0 op_sel_hi:[1,0]
	v_pk_add_f32 v[224:225], v[224:225], 1.0 op_sel_hi:[1,0]
	v_rcp_f32_e32 v210, v210
	v_rcp_f32_e32 v211, v211
	v_rcp_f32_e32 v212, v212
	v_rcp_f32_e32 v213, v213
	v_rcp_f32_e32 v214, v214
	v_rcp_f32_e32 v215, v215
	v_rcp_f32_e32 v216, v216
	v_rcp_f32_e32 v217, v217
	v_rcp_f32_e32 v218, v218
	v_rcp_f32_e32 v219, v219
	v_rcp_f32_e32 v220, v220
	v_rcp_f32_e32 v221, v221
	v_rcp_f32_e32 v222, v222
	v_rcp_f32_e32 v223, v223
	v_rcp_f32_e32 v224, v224
	v_rcp_f32_e32 v225, v225
	v_pk_fma_f32 v[14:15], v[14:15], 4.0, 4.0 op_sel_hi:[1,0,0]
	v_pk_fma_f32 v[16:17], v[16:17], 4.0, 4.0 op_sel_hi:[1,0,0]
	v_pk_fma_f32 v[10:11], v[10:11], 4.0, 4.0 op_sel_hi:[1,0,0]
	v_pk_fma_f32 v[12:13], v[12:13], 4.0, 4.0 op_sel_hi:[1,0,0]
	v_pk_fma_f32 v[6:7], v[6:7], 4.0, 4.0 op_sel_hi:[1,0,0]
	v_pk_fma_f32 v[8:9], v[8:9], 4.0, 4.0 op_sel_hi:[1,0,0]
	v_pk_fma_f32 v[2:3], v[2:3], 4.0, 4.0 op_sel_hi:[1,0,0]
	v_pk_fma_f32 v[4:5], v[4:5], 4.0, 4.0 op_sel_hi:[1,0,0]
	v_pk_mul_f32 v[38:39], v[38:39], v[210:211]
	v_pk_mul_f32 v[40:41], v[40:41], v[212:213]
	v_pk_mul_f32 v[34:35], v[34:35], v[214:215]
	v_pk_mul_f32 v[36:37], v[36:37], v[216:217]
	v_pk_mul_f32 v[22:23], v[22:23], v[218:219]
	v_pk_mul_f32 v[24:25], v[24:25], v[220:221]
	v_pk_mul_f32 v[18:19], v[18:19], v[222:223]
	v_pk_mul_f32 v[20:21], v[20:21], v[224:225]
	v_pk_mul_f32 v[38:39], v[38:39], v[14:15]
	v_pk_mul_f32 v[40:41], v[40:41], v[16:17]
	v_pk_mul_f32 v[34:35], v[34:35], v[10:11]
	v_pk_mul_f32 v[36:37], v[36:37], v[12:13]
	v_pk_mul_f32 v[22:23], v[22:23], v[6:7]
	v_pk_mul_f32 v[24:25], v[24:25], v[8:9]
	v_pk_mul_f32 v[18:19], v[18:19], v[2:3]
	v_pk_mul_f32 v[20:21], v[20:21], v[4:5]
	v_cvt_pk_fp8_f32 v244, v38, v39
	v_cvt_pk_fp8_f32 v244, v40, v41 op_sel:[0,0,1]
	v_cvt_pk_fp8_f32 v245, v34, v35
	v_cvt_pk_fp8_f32 v245, v36, v37 op_sel:[0,0,1]
	v_cvt_pk_fp8_f32 v246, v22, v23
	v_cvt_pk_fp8_f32 v246, v24, v25 op_sel:[0,0,1]
	v_cvt_pk_fp8_f32 v247, v18, v19
	v_cvt_pk_fp8_f32 v247, v20, v21 op_sel:[0,0,1]
	v_or_b32_e32 v230, v233, v173
	v_ashrrev_i32_e32 v231, 31, v230
	v_lshlrev_b64 v[230:231], 11, v[230:231]
	v_permlane16_swap_b32_e32 v244, v246
	v_permlane16_swap_b32_e32 v245, v247
	v_lshl_add_u64 v[230:231], s[16:17], 0, v[230:231]
	v_lshl_add_u64 v[230:231], v[230:231], 0, v[234:235]
	global_store_dwordx4 v[230:231], v[244:247], off
	s_and_b64 vcc, exec, s[2:3]
	s_mov_b64 s[0:1], -1
	s_cbranch_vccnz .LBB0_796
	s_andn2_b64 vcc, exec, s[12:13]
	s_cbranch_vccnz .LBB0_795
	s_nop 0
	s_branch .LBB0_795

; #define PG8_STAGEB(bufoff, gbase) glds2(voffB, (gbase), voffB, (gbase) + qstep, ldsb + (bufoff))
; #define PG8_STAGEA(bufoff, rowb, v, h, kb) do { if constexpr (GATHER) glds2((v)[h][0], Ab + (kb), (v)[h][1], Ab + (kb), ldsb + (bufoff)); \
;         else glds2(voffA, Ab + (rowb) + (h) * hstep + (kb), voffA, Ab + (rowb) + (h) * hstep + qstep + (kb), ldsb + (bufoff)); } while (0)
; #define PG8_LDA(dst, b, h) do { _Pragma("unroll") for (int m = 0; m < 4; ++m) _Pragma("unroll") for (int k = 0; k < 2; ++k) dst[m][k] = *(const PG8_LAS bf16x8*)(lds + PG8_SA(b, h) + aoff + m * 2048 + k * 1024); } while (0)
; #define PG8_LDB(dst, b, h) do { _Pragma("unroll") for (int n = 0; n < 2; ++n) _Pragma("unroll") for (int k = 0; k < 2; ++k) dst[n][k] = *(const PG8_LAS bf16x8*)(lds + PG8_SB(b, h) + boff + n * 2048 + k * 1024); } while (0)
; #define PG8_WAIT_V(n) asm volatile("s_waitcnt vmcnt(" #n ")" ::: "memory")
; #define PG8_WAIT_L(n) asm volatile("s_waitcnt lgkmcnt(" #n ")" ::: "memory")
; #define PG8_BAR __builtin_amdgcn_s_barrier()
; template <class Epi, bool GATHER, int MODE, bool SPLIT = false>
; __device__ __forceinline__ void gemm_phase(PG8_LAS unsigned char* lds, const Gemm g, const Order& S, const Epi& E) {
;     ...
;             const size_t k1 = (size_t)(t + 1) * kstep, k2 = k1 + kstep, k3 = k2 + kstep;
;             const char* b2 = cB + k2; const char* b3 = cB + k3;
;             PG8_LDB(B0, 0, 0); PG8_LDB(B1, 0, 1); PG8_SCHED; PG8_LDA(At, 0, 0); PG8_STAGEA(PG8_SA(1, 1), cAr, cv, 1, k1);
;             PG8_WAIT_V(8); PG8_WAIT_L(0); PG8_BAR; PG8_MMA(0, 0, At, B0); PG8_MMA(0, 1, At, B1); PG8_BAR; PG8_SCHED;
;             PG8_LDA(At, 0, 1); PG8_STAGEB(PG8_SB(0, 0), b2); PG8_STAGEB(PG8_SB(0, 1), b2 + hstep); PG8_STAGEA(PG8_SA(0, 0), cAr, cv, 0, k2);
;             PG8_WAIT_V(8); PG8_WAIT_L(0); PG8_BAR; PG8_MMA(1, 0, At, B0); PG8_MMA(1, 1, At, B1); PG8_BAR; PG8_SCHED;
;     ...
; #pragma unroll
;         for (int a = 0; a < 2; ++a)
; #pragma unroll
;             for (int b = 0; b < 2; ++b)
; #pragma unroll
;                 for (int m = 0; m < 4; ++m)
; #pragma unroll
;                     for (int n = 0; n < 2; ++n) acc[a][b][m][n] = (f32x4){0.f, 0.f, 0.f, 0.f};
;         cur = nxt; cB = nB; cAr = nAr; ++ui;
; #pragma unroll
;         for (int h = 0; h < 2; ++h)
; #pragma unroll
;             for (int i = 0; i < 2; ++i) cv[h][i] = nv[h][i];
;         if (wr == 1) PG8_BAR;
.LBB0_874:
	s_add_u32 s1, s31, s22
	s_addc_u32 s57, s34, s23
	s_add_u32 s15, s1, 0x40000
	s_addc_u32 s19, s57, 0
	s_add_u32 s58, s1, 0x60000
	s_addc_u32 s59, s57, 0
	s_add_u32 s60, s1, 0x20000
	s_addc_u32 s61, s57, 0
	s_mov_b32 s62, -2
	s_mov_b64 s[26:27], 0
	v_mov_b64_e32 v[34:35], 0
	v_mov_b64_e32 v[36:37], 0
	v_mov_b64_e32 v[38:39], 0
	v_mov_b64_e32 v[40:41], 0
	v_mov_b64_e32 v[42:43], 0
	v_mov_b64_e32 v[44:45], 0
	v_mov_b64_e32 v[46:47], 0
	v_mov_b64_e32 v[48:49], 0
	v_mov_b64_e32 v[50:51], 0
	v_mov_b64_e32 v[52:53], 0
	v_mov_b64_e32 v[54:55], 0
	v_mov_b64_e32 v[56:57], 0
	v_mov_b64_e32 v[58:59], 0
	v_mov_b64_e32 v[60:61], 0
	v_mov_b64_e32 v[62:63], 0
	v_mov_b64_e32 v[64:65], 0
	v_mov_b64_e32 v[66:67], 0
	v_mov_b64_e32 v[68:69], 0
	v_mov_b64_e32 v[70:71], 0
	v_mov_b64_e32 v[72:73], 0
	v_mov_b64_e32 v[74:75], 0
	v_mov_b64_e32 v[76:77], 0
	v_mov_b64_e32 v[78:79], 0
	v_mov_b64_e32 v[80:81], 0
	v_mov_b64_e32 v[82:83], 0
	v_mov_b64_e32 v[84:85], 0
	v_mov_b64_e32 v[86:87], 0
	v_mov_b64_e32 v[88:89], 0
	v_mov_b64_e32 v[90:91], 0
	v_mov_b64_e32 v[92:93], 0
	v_mov_b64_e32 v[94:95], 0
	v_mov_b64_e32 v[96:97], 0
	v_mov_b64_e32 v[98:99], 0
	v_mov_b64_e32 v[100:101], 0
	v_mov_b64_e32 v[102:103], 0
	v_mov_b64_e32 v[104:105], 0
	v_mov_b64_e32 v[106:107], 0
	v_mov_b64_e32 v[108:109], 0
	v_mov_b64_e32 v[110:111], 0
	v_mov_b64_e32 v[112:113], 0
	v_mov_b64_e32 v[114:115], 0
	v_mov_b64_e32 v[116:117], 0
	v_mov_b64_e32 v[118:119], 0
	v_mov_b64_e32 v[120:121], 0
	v_mov_b64_e32 v[122:123], 0
	v_mov_b64_e32 v[124:125], 0
	v_mov_b64_e32 v[126:127], 0
	v_mov_b64_e32 v[128:129], 0
	v_mov_b64_e32 v[130:131], 0
	v_mov_b64_e32 v[132:133], 0
	v_mov_b64_e32 v[134:135], 0
	v_mov_b64_e32 v[136:137], 0
	v_mov_b64_e32 v[138:139], 0
	v_mov_b64_e32 v[140:141], 0
	v_mov_b64_e32 v[142:143], 0
	v_mov_b64_e32 v[144:145], 0
	v_mov_b64_e32 v[146:147], 0
	v_mov_b64_e32 v[148:149], 0
	v_mov_b64_e32 v[150:151], 0
	v_mov_b64_e32 v[152:153], 0
	v_mov_b64_e32 v[154:155], 0
	v_mov_b64_e32 v[156:157], 0
	v_mov_b64_e32 v[158:159], 0
	v_mov_b64_e32 v[160:161], 0
	s_cmp_lt_u32 s40, 2
	s_cbranch_scc1 .Lp9_nobar
	s_andn2_b64 vcc, exec, s[4:5]
	s_cbranch_vccnz .Lp9_nobar
	s_barrier
.Lp9_nobar:
.LBB0_875:
	ds_read_b128 v[26:29], v172
	ds_read_b128 v[30:33], v172 offset:1024
	ds_read_b128 v[18:21], v172 offset:2048
	ds_read_b128 v[22:25], v172 offset:3072
	ds_read_b128 v[10:13], v173
	ds_read_b128 v[14:17], v173 offset:1024
	ds_read_b128 v[2:5], v173 offset:2048
	ds_read_b128 v[6:9], v173 offset:3072
	s_add_u32 s63, s24, s26
	s_addc_u32 s64, s25, s27
	s_add_u32 s28, s63, 0x100
	s_addc_u32 s29, s64, 0
	s_add_u32 s65, s15, s26
	ds_read_b128 v[180:183], v174
	ds_read_b128 v[184:187], v174 offset:1024
	ds_read_b128 v[188:191], v174 offset:2048
	ds_read_b128 v[192:195], v174 offset:3072
	ds_read_b128 v[196:199], v174 offset:4096
	ds_read_b128 v[200:203], v174 offset:5120
	ds_read_b128 v[204:207], v174 offset:6144
	ds_read_b128 v[208:211], v174 offset:7168
	s_addc_u32 s66, s19, s27
	s_add_u32 s70, s65, 0x80
	s_addc_u32 s71, s66, 0
	s_add_u32 s67, s58, s26
	s_addc_u32 s68, s59, s27
	s_add_u32 s80, s67, 0x80
	s_addc_u32 s81, s68, 0
	s_mov_b32 s69, m0
	s_mov_b32 m0, s53
	s_nop 0
	global_load_lds_dwordx4 v167, s[70:71]
	s_mov_b32 m0, s54
	s_nop 0
	global_load_lds_dwordx4 v167, s[80:81]
	s_mov_b32 m0, s69
	s_waitcnt vmcnt(8)
	s_waitcnt lgkmcnt(0)
	s_barrier
	s_setprio 1
	s_waitcnt lgkmcnt(6)
	v_mfma_f32_16x16x128_f8f6f4 v[158:161], v[26:33], v[180:187], v[158:161]
	v_mfma_f32_16x16x128_f8f6f4 v[154:157], v[18:25], v[180:187], v[154:157]
	s_waitcnt lgkmcnt(4)
	v_mfma_f32_16x16x128_f8f6f4 v[150:153], v[26:33], v[188:195], v[150:153]
	v_mfma_f32_16x16x128_f8f6f4 v[146:149], v[18:25], v[188:195], v[146:149]
	s_waitcnt lgkmcnt(2)
	v_mfma_f32_16x16x128_f8f6f4 v[142:145], v[26:33], v[196:203], v[142:145]
	v_mfma_f32_16x16x128_f8f6f4 v[138:141], v[18:25], v[196:203], v[138:141]
	s_waitcnt lgkmcnt(0)
	v_mfma_f32_16x16x128_f8f6f4 v[134:137], v[26:33], v[204:211], v[134:137]
	v_mfma_f32_16x16x128_f8f6f4 v[130:133], v[18:25], v[204:211], v[130:133]
	s_setprio 0
	s_setprio 1
	v_mfma_f32_16x16x128_f8f6f4 v[126:129], v[10:17], v[180:187], v[126:129]
	v_mfma_f32_16x16x128_f8f6f4 v[122:125], v[2:9], v[180:187], v[122:125]
	v_mfma_f32_16x16x128_f8f6f4 v[118:121], v[10:17], v[188:195], v[118:121]
	v_mfma_f32_16x16x128_f8f6f4 v[114:117], v[2:9], v[188:195], v[114:117]
	v_mfma_f32_16x16x128_f8f6f4 v[110:113], v[10:17], v[196:203], v[110:113]
	v_mfma_f32_16x16x128_f8f6f4 v[106:109], v[2:9], v[196:203], v[106:109]
	v_mfma_f32_16x16x128_f8f6f4 v[102:105], v[10:17], v[204:211], v[102:105]
	v_mfma_f32_16x16x128_f8f6f4 v[98:101], v[2:9], v[204:211], v[98:101]
	s_setprio 0
	s_barrier
	s_add_u32 s70, s63, 0x20100
	s_addc_u32 s71, s64, 0
	ds_read_b128 v[180:183], v174 offset:16384
	ds_read_b128 v[184:187], v174 offset:17408
	ds_read_b128 v[188:191], v174 offset:18432
	ds_read_b128 v[192:195], v174 offset:19456
	ds_read_b128 v[196:199], v174 offset:20480
	ds_read_b128 v[200:203], v174 offset:21504
	ds_read_b128 v[204:207], v174 offset:22528
	ds_read_b128 v[208:211], v174 offset:23552
	s_mov_b32 s69, m0
	s_mov_b32 m0, s21
	s_nop 0
	global_load_lds_dwordx4 v166, s[28:29]
	s_mov_b32 m0, s41
	s_nop 0
	global_load_lds_dwordx4 v166, s[70:71]
	s_mov_b32 m0, s69
	s_add_u32 s28, s63, 0x40100
	s_addc_u32 s29, s64, 0
	s_add_u32 s70, s63, 0x60100
	s_addc_u32 s71, s64, 0
	s_mov_b32 s69, m0
	s_mov_b32 m0, s42
	s_nop 0
	global_load_lds_dwordx4 v166, s[28:29]
	s_mov_b32 m0, s43
	s_nop 0
	global_load_lds_dwordx4 v166, s[70:71]
	s_mov_b32 m0, s69
	s_add_u32 s28, s1, s26
	s_addc_u32 s29, s57, s27
	s_add_u32 s80, s28, 0x100
	s_addc_u32 s81, s29, 0
	s_add_u32 s69, s60, s26
	s_addc_u32 s70, s61, s27
	s_add_u32 s82, s69, 0x100
	s_addc_u32 s83, s70, 0
	s_mov_b32 s71, m0
	s_mov_b32 m0, s37
	s_nop 0
	global_load_lds_dwordx4 v167, s[80:81]
	s_mov_b32 m0, s44
	s_nop 0
	global_load_lds_dwordx4 v167, s[82:83]
	s_mov_b32 m0, s71
	s_waitcnt vmcnt(8)
	s_waitcnt lgkmcnt(0)
	s_barrier
; #define PG8_STAGEB(bufoff, gbase) glds2(voffB, (gbase), voffB, (gbase) + qstep, ldsb + (bufoff))
; #define PG8_STAGEA(bufoff, rowb, v, h, kb) do { if constexpr (GATHER) glds2((v)[h][0], Ab + (kb), (v)[h][1], Ab + (kb), ldsb + (bufoff)); \
;         else glds2(voffA, Ab + (rowb) + (h) * hstep + (kb), voffA, Ab + (rowb) + (h) * hstep + qstep + (kb), ldsb + (bufoff)); } while (0)
; #define PG8_LDA(dst, b, h) do { _Pragma("unroll") for (int m = 0; m < 4; ++m) _Pragma("unroll") for (int k = 0; k < 2; ++k) dst[m][k] = *(const PG8_LAS bf16x8*)(lds + PG8_SA(b, h) + aoff + m * 2048 + k * 1024); } while (0)
; #define PG8_LDB(dst, b, h) do { _Pragma("unroll") for (int n = 0; n < 2; ++n) _Pragma("unroll") for (int k = 0; k < 2; ++k) dst[n][k] = *(const PG8_LAS bf16x8*)(lds + PG8_SB(b, h) + boff + n * 2048 + k * 1024); } while (0)
; #define PG8_WAIT_V(n) asm volatile("s_waitcnt vmcnt(" #n ")" ::: "memory")
; #define PG8_WAIT_L(n) asm volatile("s_waitcnt lgkmcnt(" #n ")" ::: "memory")
; #define PG8_BAR __builtin_amdgcn_s_barrier()
; #define PG8_SCHED __builtin_amdgcn_sched_barrier(0)
; template <class Epi, bool GATHER, int MODE, bool SPLIT = false>
; __device__ __forceinline__ void gemm_phase(PG8_LAS unsigned char* lds, const Gemm g, const Order& S, const Epi& E) {
;     ...
;             PG8_LDA(At, 0, 1); PG8_STAGEB(PG8_SB(0, 0), b2); PG8_STAGEB(PG8_SB(0, 1), b2 + hstep); PG8_STAGEA(PG8_SA(0, 0), cAr, cv, 0, k2);
;             PG8_WAIT_V(8); PG8_WAIT_L(0); PG8_BAR; PG8_MMA(1, 0, At, B0); PG8_MMA(1, 1, At, B1); PG8_BAR; PG8_SCHED;
;             PG8_LDB(B0, 1, 0); PG8_LDB(B1, 1, 1); PG8_SCHED; PG8_LDA(At, 1, 0); PG8_STAGEA(PG8_SA(0, 1), cAr, cv, 1, k2);
;             PG8_WAIT_V(8); PG8_WAIT_L(0); PG8_BAR; PG8_MMA(0, 0, At, B0); PG8_MMA(0, 1, At, B1); PG8_BAR; PG8_SCHED;
;             PG8_LDA(At, 1, 1); PG8_STAGEB(PG8_SB(1, 0), b3); PG8_STAGEB(PG8_SB(1, 1), b3 + hstep); PG8_STAGEA(PG8_SA(1, 0), cAr, cv, 0, k3);
;             PG8_WAIT_V(8); PG8_WAIT_L(0); PG8_BAR; PG8_MMA(1, 0, At, B0); PG8_MMA(1, 1, At, B1); PG8_BAR; PG8_SCHED;
	s_setprio 1
	s_waitcnt lgkmcnt(6)
	v_mfma_f32_16x16x128_f8f6f4 v[94:97], v[26:33], v[180:187], v[94:97]
	v_mfma_f32_16x16x128_f8f6f4 v[90:93], v[18:25], v[180:187], v[90:93]
	s_waitcnt lgkmcnt(4)
	v_mfma_f32_16x16x128_f8f6f4 v[86:89], v[26:33], v[188:195], v[86:89]
	v_mfma_f32_16x16x128_f8f6f4 v[82:85], v[18:25], v[188:195], v[82:85]
	s_waitcnt lgkmcnt(2)
	v_mfma_f32_16x16x128_f8f6f4 v[78:81], v[26:33], v[196:203], v[78:81]
	v_mfma_f32_16x16x128_f8f6f4 v[74:77], v[18:25], v[196:203], v[74:77]
	s_waitcnt lgkmcnt(0)
	v_mfma_f32_16x16x128_f8f6f4 v[70:73], v[26:33], v[204:211], v[70:73]
	v_mfma_f32_16x16x128_f8f6f4 v[66:69], v[18:25], v[204:211], v[66:69]
	s_setprio 0
	s_setprio 1
	v_mfma_f32_16x16x128_f8f6f4 v[62:65], v[10:17], v[180:187], v[62:65]
	v_mfma_f32_16x16x128_f8f6f4 v[58:61], v[2:9], v[180:187], v[58:61]
	v_mfma_f32_16x16x128_f8f6f4 v[54:57], v[10:17], v[188:195], v[54:57]
	v_mfma_f32_16x16x128_f8f6f4 v[50:53], v[2:9], v[188:195], v[50:53]
	v_mfma_f32_16x16x128_f8f6f4 v[46:49], v[10:17], v[196:203], v[46:49]
	v_mfma_f32_16x16x128_f8f6f4 v[42:45], v[2:9], v[196:203], v[42:45]
	v_mfma_f32_16x16x128_f8f6f4 v[38:41], v[10:17], v[204:211], v[38:41]
	v_mfma_f32_16x16x128_f8f6f4 v[34:37], v[2:9], v[204:211], v[34:37]
	s_setprio 0
	s_barrier
	ds_read_b128 v[18:21], v175
	ds_read_b128 v[22:25], v175 offset:1024
	ds_read_b128 v[26:29], v175 offset:2048
	ds_read_b128 v[30:33], v175 offset:3072
	ds_read_b128 v[10:13], v176
	ds_read_b128 v[14:17], v176 offset:1024
	ds_read_b128 v[2:5], v176 offset:2048
	ds_read_b128 v[6:9], v176 offset:3072
	ds_read_b128 v[180:183], v174 offset:32768
	ds_read_b128 v[184:187], v174 offset:33792
	ds_read_b128 v[188:191], v174 offset:34816
	ds_read_b128 v[192:195], v174 offset:35840
	ds_read_b128 v[196:199], v174 offset:36864
	ds_read_b128 v[200:203], v174 offset:37888
	ds_read_b128 v[204:207], v174 offset:38912
	ds_read_b128 v[208:211], v174 offset:39936
	s_add_u32 s80, s65, 0x100
	s_addc_u32 s81, s66, 0
	s_add_u32 s66, s67, 0x100
	s_addc_u32 s67, s68, 0
	s_mov_b32 s65, m0
	s_mov_b32 m0, s45
	s_nop 0
	global_load_lds_dwordx4 v167, s[80:81]
	s_mov_b32 m0, s46
	s_nop 0
	global_load_lds_dwordx4 v167, s[66:67]
	s_mov_b32 m0, s65
	s_waitcnt vmcnt(8)
	s_waitcnt lgkmcnt(0)
	s_barrier
	s_setprio 1
	s_waitcnt lgkmcnt(6)
	v_mfma_f32_16x16x128_f8f6f4 v[158:161], v[18:25], v[180:187], v[158:161]
	v_mfma_f32_16x16x128_f8f6f4 v[154:157], v[26:33], v[180:187], v[154:157]
	s_waitcnt lgkmcnt(4)
	v_mfma_f32_16x16x128_f8f6f4 v[150:153], v[18:25], v[188:195], v[150:153]
	v_mfma_f32_16x16x128_f8f6f4 v[146:149], v[26:33], v[188:195], v[146:149]
	s_waitcnt lgkmcnt(2)
	v_mfma_f32_16x16x128_f8f6f4 v[142:145], v[18:25], v[196:203], v[142:145]
	v_mfma_f32_16x16x128_f8f6f4 v[138:141], v[26:33], v[196:203], v[138:141]
	s_waitcnt lgkmcnt(0)
	v_mfma_f32_16x16x128_f8f6f4 v[134:137], v[18:25], v[204:211], v[134:137]
	v_mfma_f32_16x16x128_f8f6f4 v[130:133], v[26:33], v[204:211], v[130:133]
	s_setprio 0
	s_setprio 1
	v_mfma_f32_16x16x128_f8f6f4 v[126:129], v[10:17], v[180:187], v[126:129]
	v_mfma_f32_16x16x128_f8f6f4 v[122:125], v[2:9], v[180:187], v[122:125]
	v_mfma_f32_16x16x128_f8f6f4 v[118:121], v[10:17], v[188:195], v[118:121]
	v_mfma_f32_16x16x128_f8f6f4 v[114:117], v[2:9], v[188:195], v[114:117]
	v_mfma_f32_16x16x128_f8f6f4 v[110:113], v[10:17], v[196:203], v[110:113]
	v_mfma_f32_16x16x128_f8f6f4 v[106:109], v[2:9], v[196:203], v[106:109]
	v_mfma_f32_16x16x128_f8f6f4 v[102:105], v[10:17], v[204:211], v[102:105]
	v_mfma_f32_16x16x128_f8f6f4 v[98:101], v[2:9], v[204:211], v[98:101]
	s_setprio 0
	s_barrier
	s_add_u32 s66, s63, 0x180
	s_addc_u32 s67, s64, 0
	s_add_u32 s80, s63, 0x20180
	s_addc_u32 s81, s64, 0
	ds_read_b128 v[180:183], v174 offset:49152
	ds_read_b128 v[184:187], v174 offset:50176
	ds_read_b128 v[188:191], v174 offset:51200
	ds_read_b128 v[192:195], v174 offset:52224
	ds_read_b128 v[196:199], v174 offset:53248
	ds_read_b128 v[200:203], v174 offset:54272
	ds_read_b128 v[204:207], v174 offset:55296
	ds_read_b128 v[208:211], v174 offset:56320
	s_mov_b32 s65, m0
	s_mov_b32 m0, s47
	s_nop 0
	global_load_lds_dwordx4 v166, s[66:67]
	s_mov_b32 m0, s48
	s_nop 0
	global_load_lds_dwordx4 v166, s[80:81]
	s_mov_b32 m0, s65
	s_add_u32 s66, s63, 0x40180
	s_addc_u32 s67, s64, 0
	s_add_u32 s80, s63, 0x60180
	s_addc_u32 s81, s64, 0
	s_add_u32 s28, s28, 0x180
	s_addc_u32 s29, s29, 0
	s_mov_b32 s63, m0
	s_mov_b32 m0, s51
	s_nop 0
	global_load_lds_dwordx4 v166, s[66:67]
	s_mov_b32 m0, s52
	s_nop 0
	global_load_lds_dwordx4 v166, s[80:81]
	s_mov_b32 m0, s63
	s_add_u32 s64, s69, 0x180
	s_addc_u32 s65, s70, 0
	s_mov_b32 s63, m0
	s_mov_b32 m0, s49
	s_nop 0
	global_load_lds_dwordx4 v167, s[28:29]
	s_mov_b32 m0, s50
	s_nop 0
	global_load_lds_dwordx4 v167, s[64:65]
	s_mov_b32 m0, s63
	s_waitcnt vmcnt(8)
	s_waitcnt lgkmcnt(0)
	s_barrier
	s_setprio 1
	s_waitcnt lgkmcnt(6)
	v_mfma_f32_16x16x128_f8f6f4 v[94:97], v[18:25], v[180:187], v[94:97]
	v_mfma_f32_16x16x128_f8f6f4 v[90:93], v[26:33], v[180:187], v[90:93]
	s_waitcnt lgkmcnt(4)
	v_mfma_f32_16x16x128_f8f6f4 v[86:89], v[18:25], v[188:195], v[86:89]
	v_mfma_f32_16x16x128_f8f6f4 v[82:85], v[26:33], v[188:195], v[82:85]
	s_waitcnt lgkmcnt(2)
	v_mfma_f32_16x16x128_f8f6f4 v[78:81], v[18:25], v[196:203], v[78:81]
	v_mfma_f32_16x16x128_f8f6f4 v[74:77], v[26:33], v[196:203], v[74:77]
	s_waitcnt lgkmcnt(0)
	v_mfma_f32_16x16x128_f8f6f4 v[70:73], v[18:25], v[204:211], v[70:73]
	v_mfma_f32_16x16x128_f8f6f4 v[66:69], v[26:33], v[204:211], v[66:69]
	s_setprio 0
	s_setprio 1
	v_mfma_f32_16x16x128_f8f6f4 v[62:65], v[10:17], v[180:187], v[62:65]
	v_mfma_f32_16x16x128_f8f6f4 v[58:61], v[2:9], v[180:187], v[58:61]
	v_mfma_f32_16x16x128_f8f6f4 v[54:57], v[10:17], v[188:195], v[54:57]
	v_mfma_f32_16x16x128_f8f6f4 v[50:53], v[2:9], v[188:195], v[50:53]
	v_mfma_f32_16x16x128_f8f6f4 v[46:49], v[10:17], v[196:203], v[46:49]
	v_mfma_f32_16x16x128_f8f6f4 v[42:45], v[2:9], v[196:203], v[42:45]
	v_mfma_f32_16x16x128_f8f6f4 v[38:41], v[10:17], v[204:211], v[38:41]
	v_mfma_f32_16x16x128_f8f6f4 v[34:37], v[2:9], v[204:211], v[34:37]
	s_setprio 0
	s_barrier
; #define PG8_STAGEB(bufoff, gbase) glds2(voffB, (gbase), voffB, (gbase) + qstep, ldsb + (bufoff))
; #define PG8_STAGEA(bufoff, rowb, v, h, kb) do { if constexpr (GATHER) glds2((v)[h][0], Ab + (kb), (v)[h][1], Ab + (kb), ldsb + (bufoff)); \
;         else glds2(voffA, Ab + (rowb) + (h) * hstep + (kb), voffA, Ab + (rowb) + (h) * hstep + qstep + (kb), ldsb + (bufoff)); } while (0)
; #define PG8_LDA(dst, b, h) do { _Pragma("unroll") for (int m = 0; m < 4; ++m) _Pragma("unroll") for (int k = 0; k < 2; ++k) dst[m][k] = *(const PG8_LAS bf16x8*)(lds + PG8_SA(b, h) + aoff + m * 2048 + k * 1024); } while (0)
; #define PG8_LDB(dst, b, h) do { _Pragma("unroll") for (int n = 0; n < 2; ++n) _Pragma("unroll") for (int k = 0; k < 2; ++k) dst[n][k] = *(const PG8_LAS bf16x8*)(lds + PG8_SB(b, h) + boff + n * 2048 + k * 1024); } while (0)
; #define PG8_WAIT_V(n) asm volatile("s_waitcnt vmcnt(" #n ")" ::: "memory")
; #define PG8_WAIT_L(n) asm volatile("s_waitcnt lgkmcnt(" #n ")" ::: "memory")
; #define PG8_BAR __builtin_amdgcn_s_barrier()
; #define PG8_SCHED __builtin_amdgcn_sched_barrier(0)
; template <class Epi, bool GATHER, int MODE, bool SPLIT = false>
; __device__ __forceinline__ void gemm_phase(PG8_LAS unsigned char* lds, const Gemm g, const Order& S, const Epi& E) {
;     ...
;         const bool has_next = S.next(ui + 1, nxt);
;         const char* nB = has_next ? (const char*)g.Bt + (size_t)nxt.e * g.bstride + (size_t)nxt.pn * tstep : cB;
;         const size_t nAr = has_next ? (size_t)nxt.pm * tstep : cAr;
;     ...
;             PG8_LDA(At, 1, 1); PG8_STAGEB(PG8_SB(1, 0), b3); PG8_STAGEB(PG8_SB(1, 1), b3 + hstep); PG8_STAGEA(PG8_SA(1, 0), cAr, cv, 0, k3);
;             PG8_WAIT_V(8); PG8_WAIT_L(0); PG8_BAR; PG8_MMA(1, 0, At, B0); PG8_MMA(1, 1, At, B1); PG8_BAR; PG8_SCHED;
;         }
;         {
;             const size_t k1 = (size_t)(nt - 1) * kstep;
;             PG8_LDB(B0, 0, 0); PG8_LDB(B1, 0, 1); PG8_SCHED; PG8_LDA(At, 0, 0); PG8_STAGEA(PG8_SA(1, 1), cAr, cv, 1, k1);
;             PG8_WAIT_V(8); PG8_WAIT_L(0); PG8_BAR; PG8_MMA(0, 0, At, B0); PG8_MMA(0, 1, At, B1); PG8_BAR; PG8_SCHED;
;             PG8_LDA(At, 0, 1); PG8_STAGEB(PG8_SB(0, 0), nB); PG8_STAGEB(PG8_SB(0, 1), nB + hstep); PG8_STAGEA(PG8_SA(0, 0), nAr, nv, 0, 0);
;             PG8_WAIT_V(8); PG8_WAIT_L(0); PG8_BAR; PG8_MMA(1, 0, At, B0); PG8_MMA(1, 1, At, B1); PG8_BAR; PG8_SCHED;
	s_add_i32 s62, s62, 2
	s_add_u32 s26, s26, 0x100
	s_addc_u32 s27, s27, 0
	s_cmp_lt_u32 s62, 12
	s_cbranch_scc1 .LBB0_875
	v_readfirstlane_b32 s18, v230
	ds_read_b128 v[26:29], v172
	ds_read_b128 v[30:33], v172 offset:1024
	ds_read_b128 v[18:21], v172 offset:2048
	ds_read_b128 v[22:25], v172 offset:3072
	ds_read_b128 v[10:13], v173
	ds_read_b128 v[14:17], v173 offset:1024
	ds_read_b128 v[2:5], v173 offset:2048
	ds_read_b128 v[6:9], v173 offset:3072
	s_ashr_i32 s19, s18, 31
	s_lshl_b64 s[26:27], s[18:19], 22
	s_add_u32 s19, s35, s26
	s_addc_u32 s28, s36, s27
	s_ashr_i32 s15, s14, 31
	s_lshl_b64 s[26:27], s[14:15], 19
	s_add_u32 s26, s19, s26
	s_addc_u32 s27, s28, s27
	s_lshl_b64 s[28:29], s[16:17], 19
	s_and_b64 s[58:59], exec, s[2:3]
	s_cselect_b32 s25, s27, s25
	s_cselect_b32 s24, s26, s24
	s_cselect_b32 s15, s29, s23
	s_cselect_b32 s17, s28, s22
	ds_read_b128 v[180:183], v174
	ds_read_b128 v[184:187], v174 offset:1024
	ds_read_b128 v[188:191], v174 offset:2048
	ds_read_b128 v[192:195], v174 offset:3072
	ds_read_b128 v[196:199], v174 offset:4096
	ds_read_b128 v[200:203], v174 offset:5120
	ds_read_b128 v[204:207], v174 offset:6144
	ds_read_b128 v[208:211], v174 offset:7168
	s_add_u32 s22, s1, 0x40780
	s_addc_u32 s23, s57, 0
	s_add_u32 s58, s1, 0x60780
	s_addc_u32 s59, s57, 0
	s_mov_b32 s1, m0
	s_mov_b32 m0, s53
	s_nop 0
	global_load_lds_dwordx4 v167, s[22:23]
	s_mov_b32 m0, s54
	s_nop 0
	global_load_lds_dwordx4 v167, s[58:59]
	s_mov_b32 m0, s1
	s_waitcnt vmcnt(8)
	s_waitcnt lgkmcnt(0)
	s_barrier
	s_setprio 1
	s_waitcnt lgkmcnt(6)
	v_mfma_f32_16x16x128_f8f6f4 v[158:161], v[26:33], v[180:187], v[158:161]
	v_mfma_f32_16x16x128_f8f6f4 v[154:157], v[18:25], v[180:187], v[154:157]
	s_waitcnt lgkmcnt(4)
	v_mfma_f32_16x16x128_f8f6f4 v[150:153], v[26:33], v[188:195], v[150:153]
	v_mfma_f32_16x16x128_f8f6f4 v[146:149], v[18:25], v[188:195], v[146:149]
	s_waitcnt lgkmcnt(2)
	v_mfma_f32_16x16x128_f8f6f4 v[142:145], v[26:33], v[196:203], v[142:145]
	v_mfma_f32_16x16x128_f8f6f4 v[138:141], v[18:25], v[196:203], v[138:141]
	s_waitcnt lgkmcnt(0)
	v_mfma_f32_16x16x128_f8f6f4 v[134:137], v[26:33], v[204:211], v[134:137]
	v_mfma_f32_16x16x128_f8f6f4 v[130:133], v[18:25], v[204:211], v[130:133]
	s_setprio 0
	s_setprio 1
	v_mfma_f32_16x16x128_f8f6f4 v[126:129], v[10:17], v[180:187], v[126:129]
	v_mfma_f32_16x16x128_f8f6f4 v[122:125], v[2:9], v[180:187], v[122:125]
	v_mfma_f32_16x16x128_f8f6f4 v[118:121], v[10:17], v[188:195], v[118:121]
	v_mfma_f32_16x16x128_f8f6f4 v[114:117], v[2:9], v[188:195], v[114:117]
	v_mfma_f32_16x16x128_f8f6f4 v[110:113], v[10:17], v[196:203], v[110:113]
	v_mfma_f32_16x16x128_f8f6f4 v[106:109], v[2:9], v[196:203], v[106:109]
	v_mfma_f32_16x16x128_f8f6f4 v[102:105], v[10:17], v[204:211], v[102:105]
	v_mfma_f32_16x16x128_f8f6f4 v[98:101], v[2:9], v[204:211], v[98:101]
	s_setprio 0
	s_barrier
	s_add_u32 s22, s24, 0x20000
	s_addc_u32 s23, s25, 0
	ds_read_b128 v[180:183], v174 offset:16384
	ds_read_b128 v[184:187], v174 offset:17408
	ds_read_b128 v[188:191], v174 offset:18432
	ds_read_b128 v[192:195], v174 offset:19456
	ds_read_b128 v[196:199], v174 offset:20480
	ds_read_b128 v[200:203], v174 offset:21504
	ds_read_b128 v[204:207], v174 offset:22528
	ds_read_b128 v[208:211], v174 offset:23552
	s_mov_b32 s1, m0
	s_mov_b32 m0, s21
	s_nop 0
	global_load_lds_dwordx4 v166, s[24:25]
	s_mov_b32 m0, s41
	s_nop 0
	global_load_lds_dwordx4 v166, s[22:23]
	s_mov_b32 m0, s1
	s_add_u32 s22, s24, 0x40000
	s_addc_u32 s23, s25, 0
	s_add_u32 s58, s24, 0x60000
	s_addc_u32 s59, s25, 0
	s_mov_b32 s1, m0
	s_mov_b32 m0, s42
	s_nop 0
	global_load_lds_dwordx4 v166, s[22:23]
	s_mov_b32 m0, s43
	s_nop 0
	global_load_lds_dwordx4 v166, s[58:59]
	s_mov_b32 m0, s1
	s_add_u32 s22, s31, s17
	s_addc_u32 s23, s34, s15
	s_add_u32 s58, s22, 0x20000
	s_addc_u32 s59, s23, 0
	s_mov_b32 s1, m0
	s_mov_b32 m0, s37
	s_nop 0
	global_load_lds_dwordx4 v167, s[22:23]
	s_mov_b32 m0, s44
	s_nop 0
	global_load_lds_dwordx4 v167, s[58:59]
	s_mov_b32 m0, s1
	s_waitcnt vmcnt(8)
	s_waitcnt lgkmcnt(0)
	s_barrier
	s_setprio 1
	s_waitcnt lgkmcnt(6)
	v_mfma_f32_16x16x128_f8f6f4 v[94:97], v[26:33], v[180:187], v[94:97]
	v_mfma_f32_16x16x128_f8f6f4 v[90:93], v[18:25], v[180:187], v[90:93]
	s_waitcnt lgkmcnt(4)
	v_mfma_f32_16x16x128_f8f6f4 v[86:89], v[26:33], v[188:195], v[86:89]
	v_mfma_f32_16x16x128_f8f6f4 v[82:85], v[18:25], v[188:195], v[82:85]
	s_waitcnt lgkmcnt(2)
	v_mfma_f32_16x16x128_f8f6f4 v[78:81], v[26:33], v[196:203], v[78:81]
	v_mfma_f32_16x16x128_f8f6f4 v[74:77], v[18:25], v[196:203], v[74:77]
	s_waitcnt lgkmcnt(0)
	v_mfma_f32_16x16x128_f8f6f4 v[70:73], v[26:33], v[204:211], v[70:73]
	v_mfma_f32_16x16x128_f8f6f4 v[66:69], v[18:25], v[204:211], v[66:69]
	s_setprio 0
	s_setprio 1
	v_mfma_f32_16x16x128_f8f6f4 v[62:65], v[10:17], v[180:187], v[62:65]
	v_mfma_f32_16x16x128_f8f6f4 v[58:61], v[2:9], v[180:187], v[58:61]
	v_mfma_f32_16x16x128_f8f6f4 v[54:57], v[10:17], v[188:195], v[54:57]
	v_mfma_f32_16x16x128_f8f6f4 v[50:53], v[2:9], v[188:195], v[50:53]
	v_mfma_f32_16x16x128_f8f6f4 v[46:49], v[10:17], v[196:203], v[46:49]
	v_mfma_f32_16x16x128_f8f6f4 v[42:45], v[2:9], v[196:203], v[42:45]
	v_mfma_f32_16x16x128_f8f6f4 v[38:41], v[10:17], v[204:211], v[38:41]
	v_mfma_f32_16x16x128_f8f6f4 v[34:37], v[2:9], v[204:211], v[34:37]
	s_setprio 0
	s_barrier
; #define PG8_STAGEB(bufoff, gbase) glds2(voffB, (gbase), voffB, (gbase) + qstep, ldsb + (bufoff))
; #define PG8_STAGEA(bufoff, rowb, v, h, kb) do { if constexpr (GATHER) glds2((v)[h][0], Ab + (kb), (v)[h][1], Ab + (kb), ldsb + (bufoff)); \
;         else glds2(voffA, Ab + (rowb) + (h) * hstep + (kb), voffA, Ab + (rowb) + (h) * hstep + qstep + (kb), ldsb + (bufoff)); } while (0)
; #define PG8_LDA(dst, b, h) do { _Pragma("unroll") for (int m = 0; m < 4; ++m) _Pragma("unroll") for (int k = 0; k < 2; ++k) dst[m][k] = *(const PG8_LAS bf16x8*)(lds + PG8_SA(b, h) + aoff + m * 2048 + k * 1024); } while (0)
; #define PG8_LDB(dst, b, h) do { _Pragma("unroll") for (int n = 0; n < 2; ++n) _Pragma("unroll") for (int k = 0; k < 2; ++k) dst[n][k] = *(const PG8_LAS bf16x8*)(lds + PG8_SB(b, h) + boff + n * 2048 + k * 1024); } while (0)
; #define PG8_WAIT_V(n) asm volatile("s_waitcnt vmcnt(" #n ")" ::: "memory")
; #define PG8_WAIT_L(n) asm volatile("s_waitcnt lgkmcnt(" #n ")" ::: "memory")
; #define PG8_BAR __builtin_amdgcn_s_barrier()
; #define PG8_SCHED __builtin_amdgcn_sched_barrier(0)
; template <class Epi, bool GATHER, int MODE, bool SPLIT = false>
; __device__ __forceinline__ void gemm_phase(PG8_LAS unsigned char* lds, const Gemm g, const Order& S, const Epi& E) {
;     ...
;             PG8_LDB(B0, 1, 0); PG8_LDB(B1, 1, 1); PG8_SCHED; PG8_LDA(At, 1, 0); PG8_STAGEA(PG8_SA(0, 1), nAr, nv, 1, 0);
;             PG8_WAIT_V(8); PG8_WAIT_L(0); PG8_BAR; PG8_MMA(0, 0, At, B0); PG8_MMA(0, 1, At, B1); PG8_BAR; PG8_SCHED;
;             PG8_LDA(At, 1, 1); PG8_STAGEB(PG8_SB(1, 0), nB + kstep); PG8_STAGEB(PG8_SB(1, 1), nB + hstep + kstep); PG8_STAGEA(PG8_SA(1, 0), nAr, nv, 0, kstep);
;             PG8_WAIT_V(8); PG8_WAIT_L(0); PG8_BAR; PG8_MMA(1, 0, At, B0); PG8_MMA(1, 1, At, B1); PG8_BAR; PG8_SCHED;
;         }
;         if (wr == 0) PG8_BAR;
	ds_read_b128 v[26:29], v175
	ds_read_b128 v[30:33], v175 offset:1024
	ds_read_b128 v[18:21], v175 offset:2048
	ds_read_b128 v[22:25], v175 offset:3072
	ds_read_b128 v[10:13], v176
	ds_read_b128 v[14:17], v176 offset:1024
	ds_read_b128 v[2:5], v176 offset:2048
	ds_read_b128 v[6:9], v176 offset:3072
	ds_read_b128 v[180:183], v174 offset:32768
	ds_read_b128 v[184:187], v174 offset:33792
	ds_read_b128 v[188:191], v174 offset:34816
	ds_read_b128 v[192:195], v174 offset:35840
	ds_read_b128 v[196:199], v174 offset:36864
	ds_read_b128 v[200:203], v174 offset:37888
	ds_read_b128 v[204:207], v174 offset:38912
	ds_read_b128 v[208:211], v174 offset:39936
	s_add_u32 s58, s22, 0x40000
	s_addc_u32 s59, s23, 0
	s_add_u32 s60, s22, 0x60000
	s_addc_u32 s61, s23, 0
	s_mov_b32 s1, m0
	s_mov_b32 m0, s45
	s_nop 0
	global_load_lds_dwordx4 v167, s[58:59]
	s_mov_b32 m0, s46
	s_nop 0
	global_load_lds_dwordx4 v167, s[60:61]
	s_mov_b32 m0, s1
	s_waitcnt vmcnt(8)
	s_waitcnt lgkmcnt(0)
	s_barrier
	s_setprio 1
	s_waitcnt lgkmcnt(6)
	v_mfma_f32_16x16x128_f8f6f4 v[158:161], v[26:33], v[180:187], v[158:161]
	v_mfma_f32_16x16x128_f8f6f4 v[154:157], v[18:25], v[180:187], v[154:157]
	s_waitcnt lgkmcnt(4)
	v_mfma_f32_16x16x128_f8f6f4 v[150:153], v[26:33], v[188:195], v[150:153]
	v_mfma_f32_16x16x128_f8f6f4 v[146:149], v[18:25], v[188:195], v[146:149]
	s_waitcnt lgkmcnt(2)
	v_mfma_f32_16x16x128_f8f6f4 v[142:145], v[26:33], v[196:203], v[142:145]
	v_mfma_f32_16x16x128_f8f6f4 v[138:141], v[18:25], v[196:203], v[138:141]
	s_waitcnt lgkmcnt(0)
	v_mfma_f32_16x16x128_f8f6f4 v[134:137], v[26:33], v[204:211], v[134:137]
	v_mfma_f32_16x16x128_f8f6f4 v[130:133], v[18:25], v[204:211], v[130:133]
	s_setprio 0
	s_setprio 1
	v_mfma_f32_16x16x128_f8f6f4 v[126:129], v[10:17], v[180:187], v[126:129]
	v_mfma_f32_16x16x128_f8f6f4 v[122:125], v[2:9], v[180:187], v[122:125]
	v_mfma_f32_16x16x128_f8f6f4 v[118:121], v[10:17], v[188:195], v[118:121]
	v_mfma_f32_16x16x128_f8f6f4 v[114:117], v[2:9], v[188:195], v[114:117]
	v_mfma_f32_16x16x128_f8f6f4 v[110:113], v[10:17], v[196:203], v[110:113]
	v_mfma_f32_16x16x128_f8f6f4 v[106:109], v[2:9], v[196:203], v[106:109]
	v_mfma_f32_16x16x128_f8f6f4 v[102:105], v[10:17], v[204:211], v[102:105]
	v_mfma_f32_16x16x128_f8f6f4 v[98:101], v[2:9], v[204:211], v[98:101]
	s_setprio 0
	s_barrier
	s_add_u32 s58, s24, 0x80
	s_addc_u32 s59, s25, 0
	s_add_u32 s60, s24, 0x20080
	s_addc_u32 s61, s25, 0
	ds_read_b128 v[180:183], v174 offset:49152
	ds_read_b128 v[184:187], v174 offset:50176
	ds_read_b128 v[188:191], v174 offset:51200
	ds_read_b128 v[192:195], v174 offset:52224
	ds_read_b128 v[196:199], v174 offset:53248
	ds_read_b128 v[200:203], v174 offset:54272
	ds_read_b128 v[204:207], v174 offset:55296
	ds_read_b128 v[208:211], v174 offset:56320
	s_mov_b32 s1, m0
	s_mov_b32 m0, s47
	s_nop 0
	global_load_lds_dwordx4 v166, s[58:59]
	s_mov_b32 m0, s48
	s_nop 0
	global_load_lds_dwordx4 v166, s[60:61]
	s_mov_b32 m0, s1
	s_add_u32 s58, s24, 0x40080
	s_addc_u32 s59, s25, 0
	s_add_u32 s24, s24, 0x60080
	s_addc_u32 s25, s25, 0
	s_mov_b32 s1, m0
	s_mov_b32 m0, s51
	s_nop 0
	global_load_lds_dwordx4 v166, s[58:59]
	s_mov_b32 m0, s52
	s_nop 0
	global_load_lds_dwordx4 v166, s[24:25]
	s_mov_b32 m0, s1
	s_add_u32 s24, s22, 0x80
	s_addc_u32 s25, s23, 0
	s_add_u32 s22, s22, 0x20080
	s_addc_u32 s23, s23, 0
	s_mov_b32 s1, m0
	s_mov_b32 m0, s49
	s_nop 0
	global_load_lds_dwordx4 v167, s[24:25]
	s_mov_b32 m0, s50
	s_nop 0
	global_load_lds_dwordx4 v167, s[22:23]
	s_mov_b32 m0, s1
	s_waitcnt vmcnt(8)
	s_waitcnt lgkmcnt(0)
	s_barrier
	s_setprio 1
	s_waitcnt lgkmcnt(6)
	v_mfma_f32_16x16x128_f8f6f4 v[94:97], v[26:33], v[180:187], v[94:97]
	v_mfma_f32_16x16x128_f8f6f4 v[90:93], v[18:25], v[180:187], v[90:93]
	s_waitcnt lgkmcnt(4)
	v_mfma_f32_16x16x128_f8f6f4 v[86:89], v[26:33], v[188:195], v[86:89]
	v_mfma_f32_16x16x128_f8f6f4 v[82:85], v[18:25], v[188:195], v[82:85]
	s_waitcnt lgkmcnt(2)
	v_mfma_f32_16x16x128_f8f6f4 v[78:81], v[26:33], v[196:203], v[78:81]
	v_mfma_f32_16x16x128_f8f6f4 v[74:77], v[18:25], v[196:203], v[74:77]
	s_waitcnt lgkmcnt(0)
	v_mfma_f32_16x16x128_f8f6f4 v[70:73], v[26:33], v[204:211], v[70:73]
	v_mfma_f32_16x16x128_f8f6f4 v[66:69], v[18:25], v[204:211], v[66:69]
	s_setprio 0
	s_setprio 1
	v_mfma_f32_16x16x128_f8f6f4 v[62:65], v[10:17], v[180:187], v[62:65]
	v_mfma_f32_16x16x128_f8f6f4 v[58:61], v[2:9], v[180:187], v[58:61]
	v_mfma_f32_16x16x128_f8f6f4 v[54:57], v[10:17], v[188:195], v[54:57]
	v_mfma_f32_16x16x128_f8f6f4 v[50:53], v[2:9], v[188:195], v[50:53]
	v_mfma_f32_16x16x128_f8f6f4 v[46:49], v[10:17], v[196:203], v[46:49]
	v_mfma_f32_16x16x128_f8f6f4 v[42:45], v[2:9], v[196:203], v[42:45]
	v_mfma_f32_16x16x128_f8f6f4 v[38:41], v[10:17], v[204:211], v[38:41]
	v_mfma_f32_16x16x128_f8f6f4 v[34:37], v[2:9], v[204:211], v[34:37]
	s_setprio 0
	s_barrier
	s_andn2_b64 vcc, exec, s[8:9]
	s_cbranch_vccnz .LBB0_878
	s_barrier
; __device__ __forceinline__ void swap16(int& x, int& y) { const auto r = __builtin_amdgcn_permlane16_swap((unsigned)x, (unsigned)y, false, false); x = (int)r[0]; y = (int)r[1]; }
;     __device__ __forceinline__ void operator()(const f32x4 (&acc)[2][2][4][2], const Unit& u, int wr, int wc, int fr, int fq) const {
;         const int row0 = u.pm * BM + wr * 64 + fr, col0 = u.pn * BM + wc * 32 + 8 * fq;
;         const float* b = bd + (size_t)u.e * D + col0;
;         f32x4 bv[2][2];
; #pragma unroll
;         for (int bj = 0; bj < 2; ++bj)
; #pragma unroll
;             for (int n = 0; n < 2; ++n) bv[bj][n] = *(const f32x4*)(b + bj * HALF + 4 * n) * oscale;
;         const float ds = descale * oscale;
;         const int colw = col0 & ~8, odd = fq & 1;
; #pragma unroll
;         for (int ai = 0; ai < 2; ++ai)
; #pragma unroll
;             for (int bj = 0; bj < 2; ++bj) {
;                 int w0[4], w1[4];
; #pragma unroll
;                 for (int m = 0; m < 4; ++m) {
;                     f32x4 o0 = acc[ai][bj][m][0] * ds + bv[bj][0], o1 = acc[ai][bj][m][1] * ds + bv[bj][1];
; #pragma unroll
;                     for (int j = 0; j < 4; ++j) { o0[j] = fminf(fmaxf(o0[j], -448.0f), 448.0f); o1[j] = fminf(fmaxf(o1[j], -448.0f), 448.0f); }
;                     w0[m] = __builtin_amdgcn_cvt_pk_fp8_f32(o0[0], o0[1], 0, false); w0[m] = __builtin_amdgcn_cvt_pk_fp8_f32(o0[2], o0[3], w0[m], true);
;                     w1[m] = __builtin_amdgcn_cvt_pk_fp8_f32(o1[0], o1[1], 0, false); w1[m] = __builtin_amdgcn_cvt_pk_fp8_f32(o1[2], o1[3], w1[m], true);
;                 }
; #pragma unroll
;                 for (int p = 0; p < 2; ++p) { swap16(w0[2 * p], w0[2 * p + 1]); swap16(w1[2 * p], w1[2 * p + 1]);
;                     u32x4 w; w.x = (unsigned)w0[2 * p]; w.y = (unsigned)w1[2 * p]; w.z = (unsigned)w0[2 * p + 1]; w.w = (unsigned)w1[2 * p + 1];
;                     *(u32x4*)(YS + (size_t)(row0 + ai * HALF + (2 * p + odd) * 16) * D + colw + bj * HALF) = w; }
.LBB0_878:
	s_lshl_b32 s1, s20, 8
	v_ashrrev_i32_e32 v165, 31, v164
	v_or_b32_e32 v2, s1, v171
	v_lshlrev_b64 v[4:5], 13, v[164:165]
	v_lshl_add_u64 v[4:5], s[88:89], 0, v[4:5]
	v_ashrrev_i32_e32 v3, 31, v2
	s_nop 15
	s_nop 15
	v_lshl_add_u64 v[10:11], v[2:3], 2, v[4:5]
	global_load_dwordx4 v[2:5], v[10:11], off
	global_load_dwordx4 v[6:9], v[10:11], off offset:16
	global_load_dwordx4 v[20:23], v[10:11], off offset:512
	global_load_dwordx4 v[24:27], v[10:11], off offset:528
	v_mov_b32_e32 v28, 0
	v_mov_b32_e32 v183, 0
	v_mov_b32_e32 v29, 0
	v_mov_b32_e32 v30, 0
	v_mov_b32_e32 v31, 0
	v_lshl_add_u32 v164, s0, 8, v168
	v_bitop3_b32 v10, s1, v177, v171 bitop3:0xc8
	v_ashrrev_i32_e32 v11, 31, v10
	v_mov_b32_e32 v180, 0
	v_mov_b32_e32 v181, 0
	v_mov_b32_e32 v182, 0
	s_andn2_b64 vcc, exec, s[2:3]
	s_mov_b64 s[0:1], -1
	s_waitcnt vmcnt(3)
	v_pk_mul_f32 v[18:19], v[2:3], s[10:11] op_sel_hi:[1,0]
	s_waitcnt vmcnt(2)
	v_pk_mul_f32 v[14:15], v[6:7], s[10:11] op_sel_hi:[1,0]
	s_waitcnt vmcnt(1)
	v_pk_mul_f32 v[6:7], v[22:23], s[10:11] op_sel_hi:[1,0]
	v_pk_fma_f32 v[22:23], v[158:159], s[12:13], v[18:19] op_sel_hi:[1,0,1]
	v_pk_fma_f32 v[130:131], v[130:131], s[12:13], v[14:15] op_sel_hi:[1,0,1]
	v_med3_f32 v22, v22, s56, v178
	v_med3_f32 v23, v23, s56, v178
	v_med3_f32 v130, v130, s56, v178
	v_med3_f32 v131, v131, s56, v178
	v_cvt_pk_fp8_f32 v28, v22, v23
	v_pk_mul_f32 v[16:17], v[4:5], s[10:11] op_sel_hi:[1,0]
	v_cvt_pk_fp8_f32 v183, v130, v131
	v_pk_mul_f32 v[12:13], v[8:9], s[10:11] op_sel_hi:[1,0]
	v_pk_mul_f32 v[8:9], v[20:21], s[10:11] op_sel_hi:[1,0]
	s_waitcnt vmcnt(0)
	v_pk_mul_f32 v[2:3], v[26:27], s[10:11] op_sel_hi:[1,0]
	v_pk_fma_f32 v[20:21], v[160:161], s[12:13], v[16:17] op_sel_hi:[1,0,1]
	v_pk_fma_f32 v[26:27], v[154:155], s[12:13], v[14:15] op_sel_hi:[1,0,1]
	v_pk_fma_f32 v[150:151], v[150:151], s[12:13], v[18:19] op_sel_hi:[1,0,1]
	v_pk_fma_f32 v[146:147], v[146:147], s[12:13], v[14:15] op_sel_hi:[1,0,1]
	v_pk_fma_f32 v[132:133], v[132:133], s[12:13], v[12:13] op_sel_hi:[1,0,1]
	v_med3_f32 v26, v26, s56, v178
	v_med3_f32 v27, v27, s56, v178
	v_med3_f32 v20, v20, s56, v178
	v_med3_f32 v21, v21, s56, v178
	v_med3_f32 v150, v150, s56, v178
	v_med3_f32 v146, v146, s56, v178
	v_med3_f32 v151, v151, s56, v178
	v_med3_f32 v147, v147, s56, v178
	v_med3_f32 v132, v132, s56, v178
	v_cvt_pk_fp8_f32 v29, v26, v27
	v_cvt_pk_fp8_f32 v30, v150, v151
	v_cvt_pk_fp8_f32 v31, v146, v147
	v_cvt_pk_fp8_f32 v28, v20, v21 op_sel:[0,0,1]
	v_med3_f32 v20, v133, s56, v178
	v_cvt_pk_fp8_f32 v183, v132, v20 op_sel:[0,0,1]
	v_or_b32_e32 v20, v164, v169
	v_pk_mul_f32 v[4:5], v[24:25], s[10:11] op_sel_hi:[1,0]
	v_pk_fma_f32 v[24:25], v[156:157], s[12:13], v[12:13] op_sel_hi:[1,0,1]
	v_pk_fma_f32 v[32:33], v[152:153], s[12:13], v[16:17] op_sel_hi:[1,0,1]
	v_pk_fma_f32 v[148:149], v[148:149], s[12:13], v[12:13] op_sel_hi:[1,0,1]
	v_ashrrev_i32_e32 v21, 31, v20
	v_med3_f32 v24, v24, s56, v178
	v_med3_f32 v25, v25, s56, v178
	v_med3_f32 v32, v32, s56, v178
	v_med3_f32 v148, v148, s56, v178
	v_med3_f32 v33, v33, s56, v178
	v_med3_f32 v149, v149, s56, v178
	v_lshlrev_b64 v[20:21], 11, v[20:21]
	v_cvt_pk_fp8_f32 v29, v24, v25 op_sel:[0,0,1]
	v_cvt_pk_fp8_f32 v30, v32, v33 op_sel:[0,0,1]
	v_cvt_pk_fp8_f32 v31, v148, v149 op_sel:[0,0,1]
	v_lshl_add_u64 v[20:21], s[6:7], 0, v[20:21]
	v_lshl_add_u64 v[32:33], v[20:21], 0, v[10:11]
	v_or_b32_e32 v20, v164, v170
	v_ashrrev_i32_e32 v21, 31, v20
	v_lshlrev_b64 v[20:21], 11, v[20:21]
	v_permlane16_swap_b32_e32 v28, v30
	v_permlane16_swap_b32_e32 v29, v31
	v_lshl_add_u64 v[20:21], s[6:7], 0, v[20:21]
	global_store_dwordx4 v[32:33], v[28:31], off
	v_pk_fma_f32 v[22:23], v[128:129], s[12:13], v[6:7] op_sel_hi:[1,0,1]
	v_pk_fma_f32 v[26:27], v[122:123], s[12:13], v[4:5] op_sel_hi:[1,0,1]
	v_lshl_add_u64 v[28:29], v[20:21], 0, v[10:11]
	v_pk_fma_f32 v[20:21], v[126:127], s[12:13], v[8:9] op_sel_hi:[1,0,1]
	v_med3_f32 v26, v26, s56, v178
	v_med3_f32 v30, v20, s56, v178
	v_med3_f32 v21, v21, s56, v178
	v_mov_b32_e32 v20, 0
	v_cvt_pk_fp8_f32 v20, v30, v21
	v_med3_f32 v27, v27, s56, v178
	v_med3_f32 v22, v22, s56, v178
	v_mov_b32_e32 v21, 0
	v_med3_f32 v23, v23, s56, v178
	v_cvt_pk_fp8_f32 v21, v26, v27
	v_cvt_pk_fp8_f32 v20, v22, v23 op_sel:[0,0,1]
	v_pk_fma_f32 v[22:23], v[118:119], s[12:13], v[8:9] op_sel_hi:[1,0,1]
	v_pk_fma_f32 v[30:31], v[114:115], s[12:13], v[4:5] op_sel_hi:[1,0,1]
	v_med3_f32 v114, v22, s56, v178
	v_med3_f32 v23, v23, s56, v178
	v_mov_b32_e32 v22, 0
	v_pk_fma_f32 v[24:25], v[124:125], s[12:13], v[2:3] op_sel_hi:[1,0,1]
	v_cvt_pk_fp8_f32 v22, v114, v23
	v_med3_f32 v24, v24, s56, v178
	v_med3_f32 v25, v25, s56, v178
	v_cvt_pk_fp8_f32 v21, v24, v25 op_sel:[0,0,1]
	v_pk_fma_f32 v[24:25], v[120:121], s[12:13], v[6:7] op_sel_hi:[1,0,1]
	v_med3_f32 v30, v30, s56, v178
	v_med3_f32 v31, v31, s56, v178
	v_med3_f32 v24, v24, s56, v178
	v_mov_b32_e32 v23, 0
	v_med3_f32 v25, v25, s56, v178
	v_cvt_pk_fp8_f32 v23, v30, v31
	v_cvt_pk_fp8_f32 v22, v24, v25 op_sel:[0,0,1]
	v_pk_fma_f32 v[24:25], v[110:111], s[12:13], v[8:9] op_sel_hi:[1,0,1]
	v_pk_fma_f32 v[30:31], v[108:109], s[12:13], v[2:3] op_sel_hi:[1,0,1]
	v_med3_f32 v108, v24, s56, v178
	v_med3_f32 v25, v25, s56, v178
	v_mov_b32_e32 v24, 0
	v_pk_fma_f32 v[26:27], v[116:117], s[12:13], v[2:3] op_sel_hi:[1,0,1]
	v_cvt_pk_fp8_f32 v24, v108, v25
	v_med3_f32 v26, v26, s56, v178
	v_med3_f32 v27, v27, s56, v178
	v_cvt_pk_fp8_f32 v23, v26, v27 op_sel:[0,0,1]
	v_pk_fma_f32 v[26:27], v[112:113], s[12:13], v[6:7] op_sel_hi:[1,0,1]
	v_pk_fma_f32 v[106:107], v[106:107], s[12:13], v[4:5] op_sel_hi:[1,0,1]
	v_med3_f32 v26, v26, s56, v178
	v_med3_f32 v27, v27, s56, v178
; __device__ __forceinline__ void swap16(int& x, int& y) { const auto r = __builtin_amdgcn_permlane16_swap((unsigned)x, (unsigned)y, false, false); x = (int)r[0]; y = (int)r[1]; }
;     __device__ __forceinline__ void operator()(const f32x4 (&acc)[2][2][4][2], const Unit& u, int wr, int wc, int fr, int fq) const {
;     ...
;                 for (int m = 0; m < 4; ++m) {
;                     f32x4 o0 = acc[ai][bj][m][0] * ds + bv[bj][0], o1 = acc[ai][bj][m][1] * ds + bv[bj][1];
; #pragma unroll
;                     for (int j = 0; j < 4; ++j) { o0[j] = fminf(fmaxf(o0[j], -448.0f), 448.0f); o1[j] = fminf(fmaxf(o1[j], -448.0f), 448.0f); }
;                     w0[m] = __builtin_amdgcn_cvt_pk_fp8_f32(o0[0], o0[1], 0, false); w0[m] = __builtin_amdgcn_cvt_pk_fp8_f32(o0[2], o0[3], w0[m], true);
;                     w1[m] = __builtin_amdgcn_cvt_pk_fp8_f32(o1[0], o1[1], 0, false); w1[m] = __builtin_amdgcn_cvt_pk_fp8_f32(o1[2], o1[3], w1[m], true);
;                 }
; #pragma unroll
;                 for (int p = 0; p < 2; ++p) { swap16(w0[2 * p], w0[2 * p + 1]); swap16(w1[2 * p], w1[2 * p + 1]);
;                     u32x4 w; w.x = (unsigned)w0[2 * p]; w.y = (unsigned)w1[2 * p]; w.z = (unsigned)w0[2 * p + 1]; w.w = (unsigned)w1[2 * p + 1];
;                     *(u32x4*)(YS + (size_t)(row0 + ai * HALF + (2 * p + odd) * 16) * D + colw + bj * HALF) = w; }
	v_med3_f32 v106, v106, s56, v178
	v_med3_f32 v107, v107, s56, v178
	v_mov_b32_e32 v25, 0
	v_cvt_pk_fp8_f32 v24, v26, v27 op_sel:[0,0,1]
	v_pk_fma_f32 v[26:27], v[102:103], s[12:13], v[8:9] op_sel_hi:[1,0,1]
	v_pk_fma_f32 v[142:143], v[142:143], s[12:13], v[18:19] op_sel_hi:[1,0,1]
	v_pk_fma_f32 v[138:139], v[138:139], s[12:13], v[14:15] op_sel_hi:[1,0,1]
	v_pk_fma_f32 v[134:135], v[134:135], s[12:13], v[18:19] op_sel_hi:[1,0,1]
	v_cvt_pk_fp8_f32 v25, v106, v107
	v_pk_fma_f32 v[98:99], v[98:99], s[12:13], v[4:5] op_sel_hi:[1,0,1]
	v_med3_f32 v102, v26, s56, v178
	v_med3_f32 v27, v27, s56, v178
	v_mov_b32_e32 v26, 0
	v_med3_f32 v142, v142, s56, v178
	v_med3_f32 v138, v138, s56, v178
	v_med3_f32 v143, v143, s56, v178
	v_med3_f32 v139, v139, s56, v178
	v_med3_f32 v134, v134, s56, v178
	v_med3_f32 v135, v135, s56, v178
	v_med3_f32 v98, v98, s56, v178
	v_med3_f32 v99, v99, s56, v178
	v_cvt_pk_fp8_f32 v26, v102, v27
	v_mov_b32_e32 v27, 0
	v_cvt_pk_fp8_f32 v180, v142, v143
	v_cvt_pk_fp8_f32 v181, v138, v139
	v_cvt_pk_fp8_f32 v182, v134, v135
	v_cvt_pk_fp8_f32 v27, v98, v99
	v_med3_f32 v30, v30, s56, v178
	v_med3_f32 v31, v31, s56, v178
	v_pk_fma_f32 v[144:145], v[144:145], s[12:13], v[16:17] op_sel_hi:[1,0,1]
	v_pk_fma_f32 v[140:141], v[140:141], s[12:13], v[12:13] op_sel_hi:[1,0,1]
	v_pk_fma_f32 v[136:137], v[136:137], s[12:13], v[16:17] op_sel_hi:[1,0,1]
	v_cvt_pk_fp8_f32 v25, v30, v31 op_sel:[0,0,1]
	v_pk_fma_f32 v[30:31], v[104:105], s[12:13], v[6:7] op_sel_hi:[1,0,1]
	v_pk_fma_f32 v[100:101], v[100:101], s[12:13], v[2:3] op_sel_hi:[1,0,1]
	v_med3_f32 v144, v144, s56, v178
	v_med3_f32 v140, v140, s56, v178
	v_med3_f32 v145, v145, s56, v178
	v_med3_f32 v141, v141, s56, v178
	v_med3_f32 v136, v136, s56, v178
	v_med3_f32 v137, v137, s56, v178
	v_med3_f32 v30, v30, s56, v178
	v_med3_f32 v100, v100, s56, v178
	v_med3_f32 v31, v31, s56, v178
	v_med3_f32 v98, v101, s56, v178
	v_cvt_pk_fp8_f32 v180, v144, v145 op_sel:[0,0,1]
	v_cvt_pk_fp8_f32 v181, v140, v141 op_sel:[0,0,1]
	v_cvt_pk_fp8_f32 v182, v136, v137 op_sel:[0,0,1]
	v_cvt_pk_fp8_f32 v26, v30, v31 op_sel:[0,0,1]
	v_cvt_pk_fp8_f32 v27, v100, v98 op_sel:[0,0,1]
	v_permlane16_swap_b32_e32 v20, v22
	v_permlane16_swap_b32_e32 v21, v23
	v_permlane16_swap_b32_e32 v180, v182
	v_permlane16_swap_b32_e32 v181, v183
	global_store_dwordx4 v[32:33], v[20:23], off offset:128
	v_permlane16_swap_b32_e32 v24, v26
	v_permlane16_swap_b32_e32 v25, v27
	v_pk_fma_f32 v[20:21], v[94:95], s[12:13], v[18:19] op_sel_hi:[1,0,1]
	global_store_dwordx4 v[28:29], v[180:183], off
	global_store_dwordx4 v[28:29], v[24:27], off offset:128
	v_med3_f32 v28, v20, s56, v178
	v_med3_f32 v21, v21, s56, v178
	v_mov_b32_e32 v20, 0
	v_cvt_pk_fp8_f32 v20, v28, v21
	v_pk_fma_f32 v[22:23], v[96:97], s[12:13], v[16:17] op_sel_hi:[1,0,1]
	v_pk_fma_f32 v[26:27], v[90:91], s[12:13], v[14:15] op_sel_hi:[1,0,1]
	v_med3_f32 v22, v22, s56, v178
	v_med3_f32 v26, v26, s56, v178
	v_med3_f32 v27, v27, s56, v178
	v_mov_b32_e32 v21, 0
	v_med3_f32 v23, v23, s56, v178
	v_cvt_pk_fp8_f32 v21, v26, v27
	v_cvt_pk_fp8_f32 v20, v22, v23 op_sel:[0,0,1]
	v_pk_fma_f32 v[22:23], v[86:87], s[12:13], v[18:19] op_sel_hi:[1,0,1]
	v_pk_fma_f32 v[24:25], v[92:93], s[12:13], v[12:13] op_sel_hi:[1,0,1]
	v_med3_f32 v30, v22, s56, v178
	v_med3_f32 v23, v23, s56, v178
	v_mov_b32_e32 v22, 0
	v_cvt_pk_fp8_f32 v22, v30, v23
	v_med3_f32 v24, v24, s56, v178
	v_med3_f32 v25, v25, s56, v178
	v_cvt_pk_fp8_f32 v21, v24, v25 op_sel:[0,0,1]
	v_pk_fma_f32 v[24:25], v[88:89], s[12:13], v[16:17] op_sel_hi:[1,0,1]
	v_pk_fma_f32 v[28:29], v[82:83], s[12:13], v[14:15] op_sel_hi:[1,0,1]
	v_med3_f32 v24, v24, s56, v178
	v_med3_f32 v28, v28, s56, v178
	v_med3_f32 v29, v29, s56, v178
	v_mov_b32_e32 v23, 0
	v_med3_f32 v25, v25, s56, v178
	v_cvt_pk_fp8_f32 v23, v28, v29
	v_cvt_pk_fp8_f32 v22, v24, v25 op_sel:[0,0,1]
	v_pk_fma_f32 v[24:25], v[78:79], s[12:13], v[18:19] op_sel_hi:[1,0,1]
	v_pk_fma_f32 v[26:27], v[84:85], s[12:13], v[12:13] op_sel_hi:[1,0,1]
	v_med3_f32 v33, v24, s56, v178
	v_med3_f32 v25, v25, s56, v178
	v_mov_b32_e32 v24, 0
	v_cvt_pk_fp8_f32 v24, v33, v25
	v_med3_f32 v26, v26, s56, v178
	v_med3_f32 v27, v27, s56, v178
	v_cvt_pk_fp8_f32 v23, v26, v27 op_sel:[0,0,1]
	v_pk_fma_f32 v[26:27], v[80:81], s[12:13], v[16:17] op_sel_hi:[1,0,1]
	v_pk_fma_f32 v[30:31], v[74:75], s[12:13], v[14:15] op_sel_hi:[1,0,1]
	v_med3_f32 v26, v26, s56, v178
	v_med3_f32 v27, v27, s56, v178
	v_pk_fma_f32 v[14:15], v[66:67], s[12:13], v[14:15] op_sel_hi:[1,0,1]
	v_cvt_pk_fp8_f32 v24, v26, v27 op_sel:[0,0,1]
	v_med3_f32 v14, v14, s56, v178
	v_med3_f32 v15, v15, s56, v178
	v_mov_b32_e32 v27, 0
	v_cvt_pk_fp8_f32 v27, v14, v15
	v_pk_fma_f32 v[28:29], v[76:77], s[12:13], v[12:13] op_sel_hi:[1,0,1]
; __device__ __forceinline__ void swap16(int& x, int& y) { const auto r = __builtin_amdgcn_permlane16_swap((unsigned)x, (unsigned)y, false, false); x = (int)r[0]; y = (int)r[1]; }
; #define PG8_BAR __builtin_amdgcn_s_barrier()
;     __device__ __forceinline__ void operator()(const f32x4 (&acc)[2][2][4][2], const Unit& u, int wr, int wc, int fr, int fq) const {
;     ...
;                 for (int m = 0; m < 4; ++m) {
;                     f32x4 o0 = acc[ai][bj][m][0] * ds + bv[bj][0], o1 = acc[ai][bj][m][1] * ds + bv[bj][1];
; #pragma unroll
;                     for (int j = 0; j < 4; ++j) { o0[j] = fminf(fmaxf(o0[j], -448.0f), 448.0f); o1[j] = fminf(fmaxf(o1[j], -448.0f), 448.0f); }
;                     w0[m] = __builtin_amdgcn_cvt_pk_fp8_f32(o0[0], o0[1], 0, false); w0[m] = __builtin_amdgcn_cvt_pk_fp8_f32(o0[2], o0[3], w0[m], true);
;                     w1[m] = __builtin_amdgcn_cvt_pk_fp8_f32(o1[0], o1[1], 0, false); w1[m] = __builtin_amdgcn_cvt_pk_fp8_f32(o1[2], o1[3], w1[m], true);
;                 }
; #pragma unroll
;                 for (int p = 0; p < 2; ++p) { swap16(w0[2 * p], w0[2 * p + 1]); swap16(w1[2 * p], w1[2 * p + 1]);
;                     u32x4 w; w.x = (unsigned)w0[2 * p]; w.y = (unsigned)w1[2 * p]; w.z = (unsigned)w0[2 * p + 1]; w.w = (unsigned)w1[2 * p + 1];
;                     *(u32x4*)(YS + (size_t)(row0 + ai * HALF + (2 * p + odd) * 16) * D + colw + bj * HALF) = w; }
; template <class Epi, bool GATHER, int MODE, bool SPLIT = false>
; __device__ __forceinline__ void gemm_phase(PG8_LAS unsigned char* lds, const Gemm g, const Order& S, const Epi& E) {
;     ...
;         if (!has_next) break;
; #pragma unroll
;         for (int a = 0; a < 2; ++a)
; #pragma unroll
;             for (int b = 0; b < 2; ++b)
; #pragma unroll
;                 for (int m = 0; m < 4; ++m)
; #pragma unroll
;                     for (int n = 0; n < 2; ++n) acc[a][b][m][n] = (f32x4){0.f, 0.f, 0.f, 0.f};
;         cur = nxt; cB = nB; cAr = nAr; ++ui;
; #pragma unroll
;         for (int h = 0; h < 2; ++h)
; #pragma unroll
;             for (int i = 0; i < 2; ++i) cv[h][i] = nv[h][i];
;         if (wr == 1) PG8_BAR;
	v_pk_fma_f32 v[12:13], v[68:69], s[12:13], v[12:13] op_sel_hi:[1,0,1]
	v_add_u32_e32 v32, 0x80, v164
	v_med3_f32 v12, v12, s56, v178
	v_med3_f32 v13, v13, s56, v178
	v_cvt_pk_fp8_f32 v27, v12, v13 op_sel:[0,0,1]
	v_or_b32_e32 v12, v32, v169
	v_ashrrev_i32_e32 v13, 31, v12
	v_pk_fma_f32 v[18:19], v[70:71], s[12:13], v[18:19] op_sel_hi:[1,0,1]
	v_lshlrev_b64 v[12:13], 11, v[12:13]
	v_med3_f32 v18, v18, s56, v178
	v_med3_f32 v19, v19, s56, v178
	v_mov_b32_e32 v26, 0
	v_lshl_add_u64 v[12:13], s[6:7], 0, v[12:13]
	v_cvt_pk_fp8_f32 v26, v18, v19
	v_lshl_add_u64 v[18:19], v[12:13], 0, v[10:11]
	v_or_b32_e32 v12, v32, v170
	v_med3_f32 v30, v30, s56, v178
	v_med3_f32 v31, v31, s56, v178
	v_mov_b32_e32 v25, 0
	v_ashrrev_i32_e32 v13, 31, v12
	v_cvt_pk_fp8_f32 v25, v30, v31
	v_lshlrev_b64 v[12:13], 11, v[12:13]
	v_permlane16_swap_b32_e32 v20, v22
	v_permlane16_swap_b32_e32 v21, v23
	v_lshl_add_u64 v[12:13], s[6:7], 0, v[12:13]
	v_pk_fma_f32 v[16:17], v[72:73], s[12:13], v[16:17] op_sel_hi:[1,0,1]
	global_store_dwordx4 v[18:19], v[20:23], off
	v_med3_f32 v28, v28, s56, v178
	v_med3_f32 v29, v29, s56, v178
	v_lshl_add_u64 v[20:21], v[12:13], 0, v[10:11]
	v_pk_fma_f32 v[10:11], v[62:63], s[12:13], v[8:9] op_sel_hi:[1,0,1]
	v_med3_f32 v16, v16, s56, v178
	v_med3_f32 v14, v17, s56, v178
	v_med3_f32 v22, v10, s56, v178
	v_med3_f32 v11, v11, s56, v178
	v_mov_b32_e32 v10, 0
	v_cvt_pk_fp8_f32 v25, v28, v29 op_sel:[0,0,1]
	v_cvt_pk_fp8_f32 v26, v16, v14 op_sel:[0,0,1]
	v_cvt_pk_fp8_f32 v10, v22, v11
	v_pk_fma_f32 v[12:13], v[64:65], s[12:13], v[6:7] op_sel_hi:[1,0,1]
	v_pk_fma_f32 v[16:17], v[58:59], s[12:13], v[4:5] op_sel_hi:[1,0,1]
	v_med3_f32 v12, v12, s56, v178
	v_med3_f32 v16, v16, s56, v178
	v_med3_f32 v17, v17, s56, v178
	v_mov_b32_e32 v11, 0
	v_med3_f32 v13, v13, s56, v178
	v_permlane16_swap_b32_e32 v24, v26
	v_permlane16_swap_b32_e32 v25, v27
	v_cvt_pk_fp8_f32 v11, v16, v17
	v_cvt_pk_fp8_f32 v10, v12, v13 op_sel:[0,0,1]
	v_pk_fma_f32 v[12:13], v[54:55], s[12:13], v[8:9] op_sel_hi:[1,0,1]
	global_store_dwordx4 v[20:21], v[24:27], off
	v_med3_f32 v13, v13, s56, v178
	v_pk_fma_f32 v[14:15], v[60:61], s[12:13], v[2:3] op_sel_hi:[1,0,1]
	v_med3_f32 v24, v12, s56, v178
	v_mov_b32_e32 v12, 0
	v_cvt_pk_fp8_f32 v12, v24, v13
	v_med3_f32 v14, v14, s56, v178
	v_med3_f32 v15, v15, s56, v178
	v_cvt_pk_fp8_f32 v11, v14, v15 op_sel:[0,0,1]
	v_pk_fma_f32 v[14:15], v[56:57], s[12:13], v[6:7] op_sel_hi:[1,0,1]
	v_pk_fma_f32 v[22:23], v[50:51], s[12:13], v[4:5] op_sel_hi:[1,0,1]
	v_med3_f32 v14, v14, s56, v178
	v_med3_f32 v22, v22, s56, v178
	v_med3_f32 v23, v23, s56, v178
	v_mov_b32_e32 v13, 0
	v_med3_f32 v15, v15, s56, v178
	v_cvt_pk_fp8_f32 v13, v22, v23
	v_cvt_pk_fp8_f32 v12, v14, v15 op_sel:[0,0,1]
	v_pk_fma_f32 v[14:15], v[46:47], s[12:13], v[8:9] op_sel_hi:[1,0,1]
	v_pk_fma_f32 v[16:17], v[52:53], s[12:13], v[2:3] op_sel_hi:[1,0,1]
	v_med3_f32 v26, v14, s56, v178
	v_med3_f32 v15, v15, s56, v178
	v_mov_b32_e32 v14, 0
	v_cvt_pk_fp8_f32 v14, v26, v15
	v_med3_f32 v16, v16, s56, v178
	v_med3_f32 v17, v17, s56, v178
	v_cvt_pk_fp8_f32 v13, v16, v17 op_sel:[0,0,1]
	v_pk_fma_f32 v[16:17], v[48:49], s[12:13], v[6:7] op_sel_hi:[1,0,1]
	v_pk_fma_f32 v[24:25], v[42:43], s[12:13], v[4:5] op_sel_hi:[1,0,1]
	v_med3_f32 v16, v16, s56, v178
	v_med3_f32 v17, v17, s56, v178
	v_pk_fma_f32 v[8:9], v[38:39], s[12:13], v[8:9] op_sel_hi:[1,0,1]
	v_pk_fma_f32 v[4:5], v[34:35], s[12:13], v[4:5] op_sel_hi:[1,0,1]
	v_med3_f32 v24, v24, s56, v178
	v_med3_f32 v25, v25, s56, v178
	v_mov_b32_e32 v15, 0
	v_cvt_pk_fp8_f32 v14, v16, v17 op_sel:[0,0,1]
	v_med3_f32 v8, v8, s56, v178
	v_med3_f32 v4, v4, s56, v178
	v_med3_f32 v9, v9, s56, v178
	v_med3_f32 v5, v5, s56, v178
	v_mov_b32_e32 v16, 0
	v_mov_b32_e32 v17, 0
	v_cvt_pk_fp8_f32 v15, v24, v25
	v_cvt_pk_fp8_f32 v16, v8, v9
	v_cvt_pk_fp8_f32 v17, v4, v5
	v_pk_fma_f32 v[22:23], v[44:45], s[12:13], v[2:3] op_sel_hi:[1,0,1]
	v_pk_fma_f32 v[6:7], v[40:41], s[12:13], v[6:7] op_sel_hi:[1,0,1]
	v_pk_fma_f32 v[2:3], v[36:37], s[12:13], v[2:3] op_sel_hi:[1,0,1]
	v_med3_f32 v22, v22, s56, v178
	v_med3_f32 v23, v23, s56, v178
	v_med3_f32 v6, v6, s56, v178
	v_med3_f32 v2, v2, s56, v178
	v_med3_f32 v4, v7, s56, v178
	v_med3_f32 v3, v3, s56, v178
	v_cvt_pk_fp8_f32 v15, v22, v23 op_sel:[0,0,1]
	v_cvt_pk_fp8_f32 v16, v6, v4 op_sel:[0,0,1]
	v_cvt_pk_fp8_f32 v17, v2, v3 op_sel:[0,0,1]
	v_permlane16_swap_b32_e32 v10, v12
	v_permlane16_swap_b32_e32 v11, v13
	v_permlane16_swap_b32_e32 v14, v16
	v_permlane16_swap_b32_e32 v15, v17
	global_store_dwordx4 v[18:19], v[10:13], off offset:128
	global_store_dwordx4 v[20:21], v[14:17], off offset:128
	s_cbranch_vccnz .LBB0_869
	s_andn2_b64 vcc, exec, s[4:5]
	s_cbranch_vccnz .LBB0_868
	s_nop 0
	s_branch .LBB0_868
